# code placement: the five GEMM K-loop heads aligned to 64 B (s_nop-filled .p2alignl); on top of m23
# speedup vs baseline: 1.0038x; 1.0038x over previous
; #define PG8_STAGE(bufoff, gbase, voff) do { _Pragma("unroll") for (int _i = 0; _i < 2; ++_i) \
;         __builtin_amdgcn_global_load_lds((const unsigned*)((const char*)(gbase) + (voff)[_i]), (LAS unsigned*)(lds + (bufoff) + ldsw + _i * 8192), 16, 0, 0); } while (0)
; #define PG8_LDA(dst, b, h) do { if constexpr (F8) { _Pragma("unroll") for (int m = 0; m < 4; ++m) dst##8[m] = PG8_LD8(lds + PG8_SA(b, h) + aoff + m * 2048); } else { \
;         _Pragma("unroll") for (int m = 0; m < 4; ++m) _Pragma("unroll") for (int k = 0; k < 2; ++k) dst[m][k] = *(const LAS bf16x8*)(lds + PG8_SA(b, h) + aoff + m * 2048 + k * 1024); } } while (0)
; #define PG8_LDB(dst, b, h) do { if constexpr (F8) { _Pragma("unroll") for (int n = 0; n < 2; ++n) dst##8[n] = PG8_LD8(lds + PG8_SB(b, h) + boff + n * 2048); } else { \
;         _Pragma("unroll") for (int n = 0; n < 2; ++n) _Pragma("unroll") for (int k = 0; k < 2; ++k) dst[n][k] = *(const LAS bf16x8*)(lds + PG8_SB(b, h) + boff + n * 2048 + k * 1024); } } while (0)
; #define PG8_MMA0(ai, bj, At, Bt) do { __builtin_amdgcn_s_setprio(1); _Pragma("unroll") for (int m = 0; m < 4; ++m) _Pragma("unroll") for (int n = 0; n < 2; ++n) \
;         asm volatile("v_mfma_f32_16x16x128_f8f6f4 %0, %1, %2, 0" : "=&v"(acc[ai][bj][m][n]) : "v"(Bt##8[n]), "v"(At##8[m])); __builtin_amdgcn_s_setprio(0); } while (0)
; #define PG8_WAIT_L(n) asm volatile("s_waitcnt lgkmcnt(" #n ")" ::: "memory")
; #define PG8_BAR __builtin_amdgcn_s_barrier()
; #define PG8_SCHED __builtin_amdgcn_sched_barrier(0)
; template <class Epi, class Sched, bool F8 = false>
; DI void gemm_phase(LAS unsigned char* lds, const int K, const Sched& S, const Epi& E) {
;     ...
;             PG8_LDB(B0, 0, 0); PG8_LDB(B1, 0, 1); PG8_SCHED; PG8_LDA(At, 0, 0); PG8_STAGE(PG8_SA(1, 1), a1, oA[1]);
;             if (last && has_next) S.a_off(nxt, tid, oA);
;             PG8_WAIT_VX(sxe); PG8_WAIT_L(0); PG8_BAR; if (F8 && t == 0) { PG8_MMA0(0, 0, At, B0); PG8_MMA0(0, 1, At, B1); } else { PG8_MMA(0, 0, At, B0); PG8_MMA(0, 1, At, B1); } PG8_BAR; PG8_SCHED;
;             PG8_LDA(At, 0, 1); PG8_STAGE(PG8_SB(0, 0), b2, voffB); PG8_STAGE(PG8_SB(0, 1), b2 + hstep, voffB); PG8_STAGE(PG8_SA(0, 0), a2, oA[0]);
;             PG8_WAIT_VX(sxe); PG8_WAIT_L(0); PG8_BAR; if (F8 && t == 0) { PG8_MMA0(1, 0, At, B0); PG8_MMA0(1, 1, At, B1); } else { PG8_MMA(1, 0, At, B0); PG8_MMA(1, 1, At, B1); } PG8_BAR; PG8_SCHED;
.LBB0_275:
	s_ashr_i32 s43, s42, 31
	s_lshl_b64 s[4:5], s[42:43], 18
	s_add_u32 s50, s61, s4
	s_addc_u32 s51, s52, s5
	s_and_b64 s[4:5], s[40:41], exec
	s_cselect_b32 s4, s51, s31
	s_cselect_b32 s5, s50, s30
	s_ashr_i32 s47, s46, 31
	s_lshl_b64 s[6:7], s[46:47], 18
	s_add_u32 s44, s53, s6
	s_addc_u32 s45, s48, s7
	s_and_b64 s[6:7], s[40:41], exec
	s_cselect_b32 s17, s45, s67
	s_cselect_b32 s43, s44, s66
	s_add_i32 s47, s83, 0xc000
	s_waitcnt vmcnt(8)
	s_waitcnt lgkmcnt(0)
	s_barrier
	s_setprio 1
	s_waitcnt lgkmcnt(0)
	v_mfma_f32_16x16x128_f8f6f4 v[158:161], v[6:13], v[38:45], 0
	v_mfma_f32_16x16x128_f8f6f4 v[150:153], v[14:21], v[38:45], 0
	v_mfma_f32_16x16x128_f8f6f4 v[142:145], v[6:13], v[46:53], 0
	v_mfma_f32_16x16x128_f8f6f4 v[134:137], v[14:21], v[46:53], 0
	v_mfma_f32_16x16x128_f8f6f4 v[126:129], v[6:13], v[54:61], 0
	v_mfma_f32_16x16x128_f8f6f4 v[118:121], v[14:21], v[54:61], 0
	v_mfma_f32_16x16x128_f8f6f4 v[110:113], v[6:13], v[62:69], 0
	v_mfma_f32_16x16x128_f8f6f4 v[102:105], v[14:21], v[62:69], 0
	s_setprio 0
	s_setprio 1
	v_mfma_f32_16x16x128_f8f6f4 v[162:165], v[22:29], v[38:45], 0
	v_mfma_f32_16x16x128_f8f6f4 v[154:157], v[30:37], v[38:45], 0
	v_mfma_f32_16x16x128_f8f6f4 v[146:149], v[22:29], v[46:53], 0
	v_mfma_f32_16x16x128_f8f6f4 v[138:141], v[30:37], v[46:53], 0
	v_mfma_f32_16x16x128_f8f6f4 v[130:133], v[22:29], v[54:61], 0
	v_mfma_f32_16x16x128_f8f6f4 v[122:125], v[30:37], v[54:61], 0
	v_mfma_f32_16x16x128_f8f6f4 v[114:117], v[22:29], v[62:69], 0
	v_mfma_f32_16x16x128_f8f6f4 v[106:109], v[30:37], v[62:69], 0
	s_setprio 0
	s_barrier
	v_lshl_add_u64 v[180:181], s[66:67], 0, v[2:3]
	s_mov_b32 m0, s78
	v_lshl_add_u64 v[38:39], v[180:181], 0, s[28:29]
	v_lshl_add_u64 v[182:183], s[66:67], 0, v[166:167]
	s_add_u32 s6, s66, 0x20100
	ds_read_b128 v[212:215], v189 offset:16384
	ds_read_b128 v[216:219], v189 offset:17408
	ds_read_b128 v[236:239], v189 offset:18432
	ds_read_b128 v[240:243], v189 offset:19456
	ds_read_b128 v[244:247], v189 offset:20480
	ds_read_b128 v[248:251], v189 offset:21504
	ds_read_b128 v[192:195], v189 offset:22528
	ds_read_b128 v[196:199], v189 offset:23552
	global_load_lds_dwordx4 v[38:39], off
	v_lshl_add_u64 v[38:39], v[182:183], 0, s[28:29]
	s_mov_b32 m0, s79
	s_addc_u32 s7, s67, 0
	global_load_lds_dwordx4 v[38:39], off
	v_lshl_add_u64 v[38:39], s[6:7], 0, v[2:3]
	s_mov_b32 m0, s81
	v_lshl_add_u64 v[184:185], s[30:31], 0, v[168:169]
	global_load_lds_dwordx4 v[38:39], off
	v_lshl_add_u64 v[38:39], s[6:7], 0, v[166:167]
	s_mov_b32 m0, s82
	v_lshl_add_u64 v[186:187], s[30:31], 0, v[172:173]
	global_load_lds_dwordx4 v[38:39], off
	v_lshl_add_u64 v[38:39], v[184:185], 0, s[28:29]
	s_mov_b32 m0, s83
	s_nop 0
	global_load_lds_dwordx4 v[38:39], off
	v_lshl_add_u64 v[38:39], v[186:187], 0, s[28:29]
	s_mov_b32 m0, s84
	s_nop 0
	global_load_lds_dwordx4 v[38:39], off
	s_waitcnt vmcnt(8)
	s_waitcnt lgkmcnt(0)
	s_barrier
	s_setprio 1
	s_waitcnt lgkmcnt(0)
	v_mfma_f32_16x16x128_f8f6f4 v[94:97], v[6:13], v[212:219], 0
	v_mfma_f32_16x16x128_f8f6f4 v[86:89], v[14:21], v[212:219], 0
	v_mfma_f32_16x16x128_f8f6f4 v[78:81], v[6:13], v[236:243], 0
	v_mfma_f32_16x16x128_f8f6f4 v[70:73], v[14:21], v[236:243], 0
	v_mfma_f32_16x16x128_f8f6f4 v[62:65], v[6:13], v[244:251], 0
	v_mfma_f32_16x16x128_f8f6f4 v[54:57], v[14:21], v[244:251], 0
	v_mfma_f32_16x16x128_f8f6f4 v[46:49], v[6:13], v[192:199], 0
	v_mfma_f32_16x16x128_f8f6f4 v[38:41], v[14:21], v[192:199], 0
	s_setprio 0
	s_setprio 1
	v_mfma_f32_16x16x128_f8f6f4 v[98:101], v[22:29], v[212:219], 0
	v_mfma_f32_16x16x128_f8f6f4 v[90:93], v[30:37], v[212:219], 0
	v_mfma_f32_16x16x128_f8f6f4 v[82:85], v[22:29], v[236:243], 0
	v_mfma_f32_16x16x128_f8f6f4 v[74:77], v[30:37], v[236:243], 0
	v_mfma_f32_16x16x128_f8f6f4 v[66:69], v[22:29], v[244:251], 0
	v_mfma_f32_16x16x128_f8f6f4 v[58:61], v[30:37], v[244:251], 0
	v_mfma_f32_16x16x128_f8f6f4 v[50:53], v[22:29], v[192:199], 0
	v_mfma_f32_16x16x128_f8f6f4 v[42:45], v[30:37], v[192:199], 0
	s_setprio 0
	s_barrier
; #define PG8_STAGE(bufoff, gbase, voff) do { _Pragma("unroll") for (int _i = 0; _i < 2; ++_i) \
;         __builtin_amdgcn_global_load_lds((const unsigned*)((const char*)(gbase) + (voff)[_i]), (LAS unsigned*)(lds + (bufoff) + ldsw + _i * 8192), 16, 0, 0); } while (0)
; #define PG8_LDA(dst, b, h) do { if constexpr (F8) { _Pragma("unroll") for (int m = 0; m < 4; ++m) dst##8[m] = PG8_LD8(lds + PG8_SA(b, h) + aoff + m * 2048); } else { \
;         _Pragma("unroll") for (int m = 0; m < 4; ++m) _Pragma("unroll") for (int k = 0; k < 2; ++k) dst[m][k] = *(const LAS bf16x8*)(lds + PG8_SA(b, h) + aoff + m * 2048 + k * 1024); } } while (0)
; #define PG8_LDB(dst, b, h) do { if constexpr (F8) { _Pragma("unroll") for (int n = 0; n < 2; ++n) dst##8[n] = PG8_LD8(lds + PG8_SB(b, h) + boff + n * 2048); } else { \
;         _Pragma("unroll") for (int n = 0; n < 2; ++n) _Pragma("unroll") for (int k = 0; k < 2; ++k) dst[n][k] = *(const LAS bf16x8*)(lds + PG8_SB(b, h) + boff + n * 2048 + k * 1024); } } while (0)
; #define PG8_MMA0(ai, bj, At, Bt) do { __builtin_amdgcn_s_setprio(1); _Pragma("unroll") for (int m = 0; m < 4; ++m) _Pragma("unroll") for (int n = 0; n < 2; ++n) \
;         asm volatile("v_mfma_f32_16x16x128_f8f6f4 %0, %1, %2, 0" : "=&v"(acc[ai][bj][m][n]) : "v"(Bt##8[n]), "v"(At##8[m])); __builtin_amdgcn_s_setprio(0); } while (0)
; template <class Epi, class Sched, bool F8 = false>
; DI void gemm_phase(LAS unsigned char* lds, const int K, const Sched& S, const Epi& E) {
;     ...
;         for (int t = 0; t < nt; t += 2) {
;             const bool last = (t == nt - 2); const int sxe = (t == 0) ? sx : 0;
;             const char* a1 = cA + (size_t)(t + 1) * kstep;
;     ...
;             PG8_WAIT_VX(sxe); PG8_WAIT_L(0); PG8_BAR; if (F8 && t == 0) { PG8_MMA0(1, 0, At, B0); PG8_MMA0(1, 1, At, B1); } else { PG8_MMA(1, 0, At, B0); PG8_MMA(1, 1, At, B1); } PG8_BAR; PG8_SCHED;
;             PG8_LDB(B0, 1, 0); PG8_LDB(B1, 1, 1); PG8_SCHED; PG8_LDA(At, 1, 0); PG8_STAGE(PG8_SA(0, 1), a2, oA[1]);
;             PG8_WAIT_V(8); PG8_WAIT_L(0); PG8_BAR; PG8_MMA(0, 0, At, B0); PG8_MMA(0, 1, At, B1); PG8_BAR; PG8_SCHED;
;             PG8_LDA(At, 1, 1); PG8_STAGE(PG8_SB(1, 0), b3, voffB); PG8_STAGE(PG8_SB(1, 1), b3 + hstep, voffB); PG8_STAGE(PG8_SA(1, 0), a3, oA[0]);
;             PG8_WAIT_V(8); PG8_WAIT_L(0); PG8_BAR; PG8_MMA(1, 0, At, B0); PG8_MMA(1, 1, At, B1); PG8_BAR; PG8_SCHED;
	v_add_u32_e32 v192, s88, v188
	v_add_u32_e32 v193, s93, v188
	ds_read_b128 v[22:25], v192
	ds_read_b128 v[26:29], v192 offset:1024
	ds_read_b128 v[30:33], v192 offset:2048
	ds_read_b128 v[34:37], v192 offset:3072
	ds_read_b128 v[6:9], v193
	ds_read_b128 v[10:13], v193 offset:1024
	ds_read_b128 v[14:17], v193 offset:2048
	ds_read_b128 v[18:21], v193 offset:3072
	s_mov_b32 m0, s85
	v_lshl_add_u64 v[220:221], v[220:221], 0, s[28:29]
	ds_read_b128 v[212:215], v189 offset:32768
	ds_read_b128 v[216:219], v189 offset:33792
	ds_read_b128 v[236:239], v189 offset:34816
	ds_read_b128 v[240:243], v189 offset:35840
	ds_read_b128 v[244:247], v189 offset:36864
	ds_read_b128 v[248:251], v189 offset:37888
	ds_read_b128 v[194:197], v189 offset:38912
	ds_read_b128 v[198:201], v189 offset:39936
	global_load_lds_dwordx4 v[220:221], off
	v_lshl_add_u64 v[220:221], v[226:227], 0, s[28:29]
	s_mov_b32 m0, s86
	s_nop 0
	global_load_lds_dwordx4 v[220:221], off
	s_waitcnt vmcnt(8)
	s_waitcnt lgkmcnt(0)
	s_barrier
	s_setprio 1
	s_waitcnt lgkmcnt(0)
	v_mfma_f32_16x16x128_f8f6f4 v[158:161], v[22:29], v[212:219], v[158:161]
	v_mfma_f32_16x16x128_f8f6f4 v[150:153], v[30:37], v[212:219], v[150:153]
	v_mfma_f32_16x16x128_f8f6f4 v[142:145], v[22:29], v[236:243], v[142:145]
	v_mfma_f32_16x16x128_f8f6f4 v[134:137], v[30:37], v[236:243], v[134:137]
	v_mfma_f32_16x16x128_f8f6f4 v[126:129], v[22:29], v[244:251], v[126:129]
	v_mfma_f32_16x16x128_f8f6f4 v[118:121], v[30:37], v[244:251], v[118:121]
	v_mfma_f32_16x16x128_f8f6f4 v[110:113], v[22:29], v[194:201], v[110:113]
	v_mfma_f32_16x16x128_f8f6f4 v[102:105], v[30:37], v[194:201], v[102:105]
	s_setprio 0
	s_setprio 1
	v_mfma_f32_16x16x128_f8f6f4 v[162:165], v[6:13], v[212:219], v[162:165]
	v_mfma_f32_16x16x128_f8f6f4 v[154:157], v[14:21], v[212:219], v[154:157]
	v_mfma_f32_16x16x128_f8f6f4 v[146:149], v[6:13], v[236:243], v[146:149]
	v_mfma_f32_16x16x128_f8f6f4 v[138:141], v[14:21], v[236:243], v[138:141]
	v_mfma_f32_16x16x128_f8f6f4 v[130:133], v[6:13], v[244:251], v[130:133]
	v_mfma_f32_16x16x128_f8f6f4 v[122:125], v[14:21], v[244:251], v[122:125]
	v_mfma_f32_16x16x128_f8f6f4 v[114:117], v[6:13], v[194:201], v[114:117]
	v_mfma_f32_16x16x128_f8f6f4 v[106:109], v[14:21], v[194:201], v[106:109]
	s_setprio 0
	s_barrier
	s_mov_b32 m0, s89
	v_lshl_add_u64 v[180:181], v[180:181], 0, s[26:27]
	s_add_u32 s6, s66, 0x20180
	ds_read_b128 v[194:197], v189 offset:49152
	ds_read_b128 v[198:201], v189 offset:50176
	ds_read_b128 v[212:215], v189 offset:51200
	ds_read_b128 v[216:219], v189 offset:52224
	ds_read_b128 v[236:239], v189 offset:53248
	ds_read_b128 v[240:243], v189 offset:54272
	ds_read_b128 v[244:247], v189 offset:55296
	ds_read_b128 v[248:251], v189 offset:56320
	global_load_lds_dwordx4 v[180:181], off
	v_lshl_add_u64 v[180:181], v[182:183], 0, s[26:27]
	s_mov_b32 m0, s90
	s_addc_u32 s7, s67, 0
	global_load_lds_dwordx4 v[180:181], off
	v_lshl_add_u64 v[180:181], s[6:7], 0, v[2:3]
	s_mov_b32 m0, s94
	s_nop 0
	global_load_lds_dwordx4 v[180:181], off
	v_lshl_add_u64 v[180:181], s[6:7], 0, v[166:167]
	s_mov_b32 m0, s95
	s_nop 0
	global_load_lds_dwordx4 v[180:181], off
	v_lshl_add_u64 v[180:181], v[184:185], 0, s[26:27]
	s_mov_b32 m0, s91
	s_nop 0
	global_load_lds_dwordx4 v[180:181], off
	v_lshl_add_u64 v[180:181], v[186:187], 0, s[26:27]
	s_mov_b32 m0, s92
	s_nop 0
	global_load_lds_dwordx4 v[180:181], off
	s_waitcnt vmcnt(8)
	s_waitcnt lgkmcnt(0)
	s_barrier
	s_setprio 1
	s_waitcnt lgkmcnt(0)
	v_mfma_f32_16x16x128_f8f6f4 v[94:97], v[22:29], v[194:201], v[94:97]
	v_mfma_f32_16x16x128_f8f6f4 v[86:89], v[30:37], v[194:201], v[86:89]
	v_mfma_f32_16x16x128_f8f6f4 v[78:81], v[22:29], v[212:219], v[78:81]
	v_mfma_f32_16x16x128_f8f6f4 v[70:73], v[30:37], v[212:219], v[70:73]
	v_mfma_f32_16x16x128_f8f6f4 v[62:65], v[22:29], v[236:243], v[62:65]
	v_mfma_f32_16x16x128_f8f6f4 v[54:57], v[30:37], v[236:243], v[54:57]
	v_mfma_f32_16x16x128_f8f6f4 v[46:49], v[22:29], v[244:251], v[46:49]
	v_mfma_f32_16x16x128_f8f6f4 v[38:41], v[30:37], v[244:251], v[38:41]
	s_setprio 0
	s_setprio 1
	v_mfma_f32_16x16x128_f8f6f4 v[98:101], v[6:13], v[194:201], v[98:101]
	v_mfma_f32_16x16x128_f8f6f4 v[90:93], v[14:21], v[194:201], v[90:93]
	v_mfma_f32_16x16x128_f8f6f4 v[82:85], v[6:13], v[212:219], v[82:85]
	v_mfma_f32_16x16x128_f8f6f4 v[74:77], v[14:21], v[212:219], v[74:77]
	v_mfma_f32_16x16x128_f8f6f4 v[66:69], v[6:13], v[236:243], v[66:69]
	v_mfma_f32_16x16x128_f8f6f4 v[58:61], v[14:21], v[236:243], v[58:61]
	v_mfma_f32_16x16x128_f8f6f4 v[50:53], v[6:13], v[244:251], v[50:53]
	v_mfma_f32_16x16x128_f8f6f4 v[42:45], v[14:21], v[244:251], v[42:45]
	s_setprio 0
	s_barrier
	s_add_u32 s6, s66, 0x200
	s_addc_u32 s7, s67, 0
	s_mov_b32 s8, 0
	.p2alignl 6, 3212836864

; #define PG8_STAGE(bufoff, gbase, voff) do { _Pragma("unroll") for (int _i = 0; _i < 2; ++_i) \
;         __builtin_amdgcn_global_load_lds((const unsigned*)((const char*)(gbase) + (voff)[_i]), (LAS unsigned*)(lds + (bufoff) + ldsw + _i * 8192), 16, 0, 0); } while (0)
; #define PG8_LDA(dst, b, h) do { if constexpr (F8) { _Pragma("unroll") for (int m = 0; m < 4; ++m) dst##8[m] = PG8_LD8(lds + PG8_SA(b, h) + aoff + m * 2048); } else { \
;         _Pragma("unroll") for (int m = 0; m < 4; ++m) _Pragma("unroll") for (int k = 0; k < 2; ++k) dst[m][k] = *(const LAS bf16x8*)(lds + PG8_SA(b, h) + aoff + m * 2048 + k * 1024); } } while (0)
; #define PG8_MMA0(ai, bj, At, Bt) do { __builtin_amdgcn_s_setprio(1); _Pragma("unroll") for (int m = 0; m < 4; ++m) _Pragma("unroll") for (int n = 0; n < 2; ++n) \
;         asm volatile("v_mfma_f32_16x16x128_f8f6f4 %0, %1, %2, 0" : "=&v"(acc[ai][bj][m][n]) : "v"(Bt##8[n]), "v"(At##8[m])); __builtin_amdgcn_s_setprio(0); } while (0)
; template <class Epi, class Sched, bool F8 = false>
; DI void gemm_phase(LAS unsigned char* lds, const int K, const Sched& S, const Epi& E) {
;     ...
;         const bool has_next = S.next(ui + 1, nxt);
;         const char* nA = has_next ? S.a_base(nxt) : cA; const char* nB = has_next ? S.b_base(nxt) : cB;
;         for (int t = 0; t < nt; t += 2) {
;             const bool last = (t == nt - 2); const int sxe = (t == 0) ? sx : 0;
;             const char* a1 = cA + (size_t)(t + 1) * kstep;
;             const char* a2 = last ? nA : cA + (size_t)(t + 2) * kstep; const char* b2 = last ? nB : cB + (size_t)(t + 2) * kstep;
;             const char* a3 = a2 + kstep; const char* b3 = b2 + kstep;
;             PG8_LDB(B0, 0, 0); PG8_LDB(B1, 0, 1); PG8_SCHED; PG8_LDA(At, 0, 0); PG8_STAGE(PG8_SA(1, 1), a1, oA[1]);
;             if (last && has_next) S.a_off(nxt, tid, oA);
;             PG8_WAIT_VX(sxe); PG8_WAIT_L(0); PG8_BAR; if (F8 && t == 0) { PG8_MMA0(0, 0, At, B0); PG8_MMA0(0, 1, At, B1); } else { PG8_MMA(0, 0, At, B0); PG8_MMA(0, 1, At, B1); } PG8_BAR; PG8_SCHED;
;             PG8_LDA(At, 0, 1); PG8_STAGE(PG8_SB(0, 0), b2, voffB); PG8_STAGE(PG8_SB(0, 1), b2 + hstep, voffB); PG8_STAGE(PG8_SA(0, 0), a2, oA[0]);
;             PG8_WAIT_VX(sxe); PG8_WAIT_L(0); PG8_BAR; if (F8 && t == 0) { PG8_MMA0(1, 0, At, B0); PG8_MMA0(1, 1, At, B1); } else { PG8_MMA(1, 0, At, B0); PG8_MMA(1, 1, At, B1); } PG8_BAR; PG8_SCHED;
.LBB0_902:
	s_ashr_i32 s49, s48, 31
	s_lshl_b64 s[6:7], s[48:49], 18
	s_add_u32 s50, s39, s6
	s_addc_u32 s51, s62, s7
	v_add_u32_e32 v188, s67, v206
	v_add_u32_e32 v189, s75, v206
	s_and_b64 s[6:7], s[40:41], exec
	ds_read_b128 v[6:9], v188
	ds_read_b128 v[10:13], v188 offset:1024
	ds_read_b128 v[14:17], v188 offset:2048
	ds_read_b128 v[18:21], v188 offset:3072
	ds_read_b128 v[22:25], v189
	ds_read_b128 v[26:29], v189 offset:1024
	ds_read_b128 v[30:33], v189 offset:2048
	ds_read_b128 v[34:37], v189 offset:3072
	s_cselect_b32 s49, s51, s57
	s_cselect_b32 s95, s50, s56
	s_ashr_i32 s47, s46, 31
	s_lshl_b64 s[6:7], s[46:47], 18
	s_add_u32 s52, s63, s6
	s_addc_u32 s53, s66, s7
	s_and_b64 s[6:7], s[40:41], exec
	v_mov_b64_e32 v[210:211], 0x10000
	v_mov_b64_e32 v[216:217], 0xffff
	v_mov_b32_e32 v203, 0x3727c5ac
	s_cselect_b32 s47, s53, s59
	s_cselect_b32 s96, s52, s58
	v_lshl_add_u64 v[200:201], s[56:57], 0, v[170:171]
	s_add_i32 s97, s79, 0xc000
	v_lshl_add_u64 v[70:71], v[200:201], 0, s[24:25]
	s_mov_b32 m0, s97
	v_lshl_add_u64 v[212:213], s[56:57], 0, v[174:175]
	s_add_i32 vcc_lo, s79, 0xe000
	ds_read_b128 v[38:41], v214
	ds_read_b128 v[42:45], v214 offset:1024
	ds_read_b128 v[46:49], v214 offset:2048
	ds_read_b128 v[50:53], v214 offset:3072
	ds_read_b128 v[54:57], v214 offset:4096
	ds_read_b128 v[58:61], v214 offset:5120
	ds_read_b128 v[62:65], v214 offset:6144
	ds_read_b128 v[66:69], v214 offset:7168
	global_load_lds_dwordx4 v[70:71], off
	v_lshl_add_u64 v[70:71], v[212:213], 0, s[24:25]
	s_mov_b32 m0, vcc_lo
	s_nop 0
	global_load_lds_dwordx4 v[70:71], off
	s_waitcnt vmcnt(8)
	s_waitcnt lgkmcnt(0)
	s_barrier
	s_setprio 1
	s_waitcnt lgkmcnt(0)
	v_mfma_f32_16x16x128_f8f6f4 v[162:165], v[6:13], v[38:45], 0
	v_mfma_f32_16x16x128_f8f6f4 v[158:161], v[14:21], v[38:45], 0
	v_mfma_f32_16x16x128_f8f6f4 v[146:149], v[6:13], v[46:53], 0
	v_mfma_f32_16x16x128_f8f6f4 v[142:145], v[14:21], v[46:53], 0
	v_mfma_f32_16x16x128_f8f6f4 v[130:133], v[6:13], v[54:61], 0
	v_mfma_f32_16x16x128_f8f6f4 v[126:129], v[14:21], v[54:61], 0
	v_mfma_f32_16x16x128_f8f6f4 v[114:117], v[6:13], v[62:69], 0
	v_mfma_f32_16x16x128_f8f6f4 v[110:113], v[14:21], v[62:69], 0
	s_setprio 0
	s_setprio 1
	v_mfma_f32_16x16x128_f8f6f4 v[154:157], v[22:29], v[38:45], 0
	v_mfma_f32_16x16x128_f8f6f4 v[150:153], v[30:37], v[38:45], 0
	v_mfma_f32_16x16x128_f8f6f4 v[138:141], v[22:29], v[46:53], 0
	v_mfma_f32_16x16x128_f8f6f4 v[134:137], v[30:37], v[46:53], 0
	v_mfma_f32_16x16x128_f8f6f4 v[122:125], v[22:29], v[54:61], 0
	v_mfma_f32_16x16x128_f8f6f4 v[118:121], v[30:37], v[54:61], 0
	v_mfma_f32_16x16x128_f8f6f4 v[98:101], v[22:29], v[62:69], 0
	v_mfma_f32_16x16x128_f8f6f4 v[94:97], v[30:37], v[62:69], 0
	s_setprio 0
	s_barrier
	v_lshl_add_u64 v[180:181], s[58:59], 0, v[2:3]
	s_mov_b32 m0, s68
	v_lshl_add_u64 v[46:47], v[180:181], 0, s[28:29]
	v_lshl_add_u64 v[182:183], s[58:59], 0, v[166:167]
	s_add_u32 s6, s58, 0x20100
	ds_read_b128 v[38:41], v214 offset:16384
	ds_read_b128 v[42:45], v214 offset:17408
	ds_read_b128 v[54:57], v214 offset:18432
	ds_read_b128 v[58:61], v214 offset:19456
	ds_read_b128 v[190:193], v214 offset:20480
	ds_read_b128 v[194:197], v214 offset:21504
	ds_read_b128 v[236:239], v214 offset:22528
	ds_read_b128 v[240:243], v214 offset:23552
	global_load_lds_dwordx4 v[46:47], off
	v_lshl_add_u64 v[46:47], v[182:183], 0, s[28:29]
	s_mov_b32 m0, s74
	s_addc_u32 s7, s59, 0
	global_load_lds_dwordx4 v[46:47], off
	v_lshl_add_u64 v[46:47], s[6:7], 0, v[2:3]
	s_mov_b32 m0, s76
	v_lshl_add_u64 v[184:185], s[56:57], 0, v[168:169]
	global_load_lds_dwordx4 v[46:47], off
	v_lshl_add_u64 v[46:47], s[6:7], 0, v[166:167]
	s_mov_b32 m0, s78
	v_lshl_add_u64 v[186:187], s[56:57], 0, v[172:173]
	global_load_lds_dwordx4 v[46:47], off
	v_lshl_add_u64 v[46:47], v[184:185], 0, s[28:29]
	s_mov_b32 m0, s79
	s_nop 0
	global_load_lds_dwordx4 v[46:47], off
	v_lshl_add_u64 v[46:47], v[186:187], 0, s[28:29]
	s_mov_b32 m0, s80
	s_nop 0
	global_load_lds_dwordx4 v[46:47], off
	s_waitcnt vmcnt(8)
	s_waitcnt lgkmcnt(0)
	s_barrier
	s_setprio 1
	s_waitcnt lgkmcnt(0)
	v_mfma_f32_16x16x128_f8f6f4 v[106:109], v[6:13], v[38:45], 0
	v_mfma_f32_16x16x128_f8f6f4 v[102:105], v[14:21], v[38:45], 0
	v_mfma_f32_16x16x128_f8f6f4 v[82:85], v[6:13], v[54:61], 0
	v_mfma_f32_16x16x128_f8f6f4 v[78:81], v[14:21], v[54:61], 0
	v_mfma_f32_16x16x128_f8f6f4 v[66:69], v[6:13], v[190:197], 0
	v_mfma_f32_16x16x128_f8f6f4 v[62:65], v[14:21], v[190:197], 0
	v_mfma_f32_16x16x128_f8f6f4 v[50:53], v[6:13], v[236:243], 0
	v_mfma_f32_16x16x128_f8f6f4 v[46:49], v[14:21], v[236:243], 0
	s_setprio 0
	s_setprio 1
	v_mfma_f32_16x16x128_f8f6f4 v[90:93], v[22:29], v[38:45], 0
	v_mfma_f32_16x16x128_f8f6f4 v[86:89], v[30:37], v[38:45], 0
	v_mfma_f32_16x16x128_f8f6f4 v[74:77], v[22:29], v[54:61], 0
	v_mfma_f32_16x16x128_f8f6f4 v[70:73], v[30:37], v[54:61], 0
	v_mfma_f32_16x16x128_f8f6f4 v[58:61], v[22:29], v[190:197], 0
	v_mfma_f32_16x16x128_f8f6f4 v[54:57], v[30:37], v[190:197], 0
	v_mfma_f32_16x16x128_f8f6f4 v[42:45], v[22:29], v[236:243], 0
	v_mfma_f32_16x16x128_f8f6f4 v[38:41], v[30:37], v[236:243], 0
	s_setprio 0
	s_barrier
; #define PG8_STAGE(bufoff, gbase, voff) do { _Pragma("unroll") for (int _i = 0; _i < 2; ++_i) \
;         __builtin_amdgcn_global_load_lds((const unsigned*)((const char*)(gbase) + (voff)[_i]), (LAS unsigned*)(lds + (bufoff) + ldsw + _i * 8192), 16, 0, 0); } while (0)
; #define PG8_LDA(dst, b, h) do { if constexpr (F8) { _Pragma("unroll") for (int m = 0; m < 4; ++m) dst##8[m] = PG8_LD8(lds + PG8_SA(b, h) + aoff + m * 2048); } else { \
;         _Pragma("unroll") for (int m = 0; m < 4; ++m) _Pragma("unroll") for (int k = 0; k < 2; ++k) dst[m][k] = *(const LAS bf16x8*)(lds + PG8_SA(b, h) + aoff + m * 2048 + k * 1024); } } while (0)
; #define PG8_LDB(dst, b, h) do { if constexpr (F8) { _Pragma("unroll") for (int n = 0; n < 2; ++n) dst##8[n] = PG8_LD8(lds + PG8_SB(b, h) + boff + n * 2048); } else { \
;         _Pragma("unroll") for (int n = 0; n < 2; ++n) _Pragma("unroll") for (int k = 0; k < 2; ++k) dst[n][k] = *(const LAS bf16x8*)(lds + PG8_SB(b, h) + boff + n * 2048 + k * 1024); } } while (0)
; #define PG8_WAIT_V(n) asm volatile("s_waitcnt vmcnt(" #n ")" ::: "memory")
; #define PG8_WAIT_L(n) asm volatile("s_waitcnt lgkmcnt(" #n ")" ::: "memory")
; #define PG8_BAR __builtin_amdgcn_s_barrier()
; #define PG8_SCHED __builtin_amdgcn_sched_barrier(0)
; template <class Epi, class Sched, bool F8 = false>
; DI void gemm_phase(LAS unsigned char* lds, const int K, const Sched& S, const Epi& E) {
;     ...
;             PG8_LDB(B0, 1, 0); PG8_LDB(B1, 1, 1); PG8_SCHED; PG8_LDA(At, 1, 0); PG8_STAGE(PG8_SA(0, 1), a2, oA[1]);
;             PG8_WAIT_V(8); PG8_WAIT_L(0); PG8_BAR; PG8_MMA(0, 0, At, B0); PG8_MMA(0, 1, At, B1); PG8_BAR; PG8_SCHED;
;             PG8_LDA(At, 1, 1); PG8_STAGE(PG8_SB(1, 0), b3, voffB); PG8_STAGE(PG8_SB(1, 1), b3 + hstep, voffB); PG8_STAGE(PG8_SA(1, 0), a3, oA[0]);
;             PG8_WAIT_V(8); PG8_WAIT_L(0); PG8_BAR; PG8_MMA(1, 0, At, B0); PG8_MMA(1, 1, At, B1); PG8_BAR; PG8_SCHED;
;         }
	v_add_u32_e32 v190, s85, v206
	v_add_u32_e32 v191, s90, v206
	ds_read_b128 v[22:25], v190
	ds_read_b128 v[26:29], v190 offset:1024
	ds_read_b128 v[30:33], v190 offset:2048
	ds_read_b128 v[34:37], v190 offset:3072
	ds_read_b128 v[6:9], v191
	ds_read_b128 v[10:13], v191 offset:1024
	ds_read_b128 v[14:17], v191 offset:2048
	ds_read_b128 v[18:21], v191 offset:3072
	s_mov_b32 m0, s81
	v_lshl_add_u64 v[200:201], v[200:201], 0, s[28:29]
	ds_read_b128 v[192:195], v214 offset:32768
	ds_read_b128 v[196:199], v214 offset:33792
	ds_read_b128 v[236:239], v214 offset:34816
	ds_read_b128 v[240:243], v214 offset:35840
	ds_read_b128 v[244:247], v214 offset:36864
	ds_read_b128 v[248:251], v214 offset:37888
	ds_read_b128 v[226:229], v214 offset:38912
	ds_read_b128 v[230:233], v214 offset:39936
	global_load_lds_dwordx4 v[200:201], off
	v_lshl_add_u64 v[200:201], v[212:213], 0, s[28:29]
	s_mov_b32 m0, s82
	s_nop 0
	global_load_lds_dwordx4 v[200:201], off
	s_waitcnt vmcnt(8)
	s_waitcnt lgkmcnt(0)
	s_barrier
	s_setprio 1
	s_waitcnt lgkmcnt(0)
	v_mfma_f32_16x16x128_f8f6f4 v[162:165], v[22:29], v[192:199], v[162:165]
	v_mfma_f32_16x16x128_f8f6f4 v[158:161], v[30:37], v[192:199], v[158:161]
	v_mfma_f32_16x16x128_f8f6f4 v[146:149], v[22:29], v[236:243], v[146:149]
	v_mfma_f32_16x16x128_f8f6f4 v[142:145], v[30:37], v[236:243], v[142:145]
	v_mfma_f32_16x16x128_f8f6f4 v[130:133], v[22:29], v[244:251], v[130:133]
	v_mfma_f32_16x16x128_f8f6f4 v[126:129], v[30:37], v[244:251], v[126:129]
	v_mfma_f32_16x16x128_f8f6f4 v[114:117], v[22:29], v[226:233], v[114:117]
	v_mfma_f32_16x16x128_f8f6f4 v[110:113], v[30:37], v[226:233], v[110:113]
	s_setprio 0
	s_setprio 1
	v_mfma_f32_16x16x128_f8f6f4 v[154:157], v[6:13], v[192:199], v[154:157]
	v_mfma_f32_16x16x128_f8f6f4 v[150:153], v[14:21], v[192:199], v[150:153]
	v_mfma_f32_16x16x128_f8f6f4 v[138:141], v[6:13], v[236:243], v[138:141]
	v_mfma_f32_16x16x128_f8f6f4 v[134:137], v[14:21], v[236:243], v[134:137]
	v_mfma_f32_16x16x128_f8f6f4 v[122:125], v[6:13], v[244:251], v[122:125]
	v_mfma_f32_16x16x128_f8f6f4 v[118:121], v[14:21], v[244:251], v[118:121]
	v_mfma_f32_16x16x128_f8f6f4 v[98:101], v[6:13], v[226:233], v[98:101]
	v_mfma_f32_16x16x128_f8f6f4 v[94:97], v[14:21], v[226:233], v[94:97]
	s_setprio 0
	s_barrier
	s_mov_b32 m0, s86
	v_lshl_add_u64 v[180:181], v[180:181], 0, s[26:27]
	s_add_u32 s6, s58, 0x20180
	ds_read_b128 v[192:195], v214 offset:49152
	ds_read_b128 v[196:199], v214 offset:50176
	ds_read_b128 v[226:229], v214 offset:51200
	ds_read_b128 v[230:233], v214 offset:52224
	ds_read_b128 v[236:239], v214 offset:53248
	ds_read_b128 v[240:243], v214 offset:54272
	ds_read_b128 v[244:247], v214 offset:55296
	ds_read_b128 v[248:251], v214 offset:56320
	global_load_lds_dwordx4 v[180:181], off
	v_lshl_add_u64 v[180:181], v[182:183], 0, s[26:27]
	s_mov_b32 m0, s87
	s_addc_u32 s7, s59, 0
	global_load_lds_dwordx4 v[180:181], off
	v_lshl_add_u64 v[180:181], s[6:7], 0, v[2:3]
	s_mov_b32 m0, s91
	s_nop 0
	global_load_lds_dwordx4 v[180:181], off
	v_lshl_add_u64 v[180:181], s[6:7], 0, v[166:167]
	s_mov_b32 m0, s92
	s_nop 0
	global_load_lds_dwordx4 v[180:181], off
	v_lshl_add_u64 v[180:181], v[184:185], 0, s[26:27]
	s_mov_b32 m0, s88
	s_nop 0
	global_load_lds_dwordx4 v[180:181], off
	v_lshl_add_u64 v[180:181], v[186:187], 0, s[26:27]
	s_mov_b32 m0, s89
	s_nop 0
	global_load_lds_dwordx4 v[180:181], off
	s_waitcnt vmcnt(8)
	s_waitcnt lgkmcnt(0)
	s_barrier
	s_setprio 1
	s_waitcnt lgkmcnt(0)
	v_mfma_f32_16x16x128_f8f6f4 v[106:109], v[22:29], v[192:199], v[106:109]
	v_mfma_f32_16x16x128_f8f6f4 v[102:105], v[30:37], v[192:199], v[102:105]
	v_mfma_f32_16x16x128_f8f6f4 v[82:85], v[22:29], v[226:233], v[82:85]
	v_mfma_f32_16x16x128_f8f6f4 v[78:81], v[30:37], v[226:233], v[78:81]
	v_mfma_f32_16x16x128_f8f6f4 v[66:69], v[22:29], v[236:243], v[66:69]
	v_mfma_f32_16x16x128_f8f6f4 v[62:65], v[30:37], v[236:243], v[62:65]
	v_mfma_f32_16x16x128_f8f6f4 v[50:53], v[22:29], v[244:251], v[50:53]
	v_mfma_f32_16x16x128_f8f6f4 v[46:49], v[30:37], v[244:251], v[46:49]
	s_setprio 0
	s_setprio 1
	v_mfma_f32_16x16x128_f8f6f4 v[90:93], v[6:13], v[192:199], v[90:93]
	v_mfma_f32_16x16x128_f8f6f4 v[86:89], v[14:21], v[192:199], v[86:89]
	v_mfma_f32_16x16x128_f8f6f4 v[74:77], v[6:13], v[226:233], v[74:77]
	v_mfma_f32_16x16x128_f8f6f4 v[70:73], v[14:21], v[226:233], v[70:73]
	v_mfma_f32_16x16x128_f8f6f4 v[58:61], v[6:13], v[236:243], v[58:61]
	v_mfma_f32_16x16x128_f8f6f4 v[54:57], v[14:21], v[236:243], v[54:57]
	v_mfma_f32_16x16x128_f8f6f4 v[42:45], v[6:13], v[244:251], v[42:45]
	v_mfma_f32_16x16x128_f8f6f4 v[38:41], v[14:21], v[244:251], v[38:41]
	s_setprio 0
	s_barrier
	s_add_u32 s6, s58, 0x200
	s_addc_u32 s7, s59, 0
	s_mov_b32 s8, 0
	.p2alignl 6, 3212836864

; #define PG8_STAGE(bufoff, gbase, voff) do { _Pragma("unroll") for (int _i = 0; _i < 2; ++_i) \
;         __builtin_amdgcn_global_load_lds((const unsigned*)((const char*)(gbase) + (voff)[_i]), (LAS unsigned*)(lds + (bufoff) + ldsw + _i * 8192), 16, 0, 0); } while (0)
; #define PG8_LDA(dst, b, h) do { if constexpr (F8) { _Pragma("unroll") for (int m = 0; m < 4; ++m) dst##8[m] = PG8_LD8(lds + PG8_SA(b, h) + aoff + m * 2048); } else { \
;         _Pragma("unroll") for (int m = 0; m < 4; ++m) _Pragma("unroll") for (int k = 0; k < 2; ++k) dst[m][k] = *(const LAS bf16x8*)(lds + PG8_SA(b, h) + aoff + m * 2048 + k * 1024); } } while (0)
; #define PG8_MMA0(ai, bj, At, Bt) do { __builtin_amdgcn_s_setprio(1); _Pragma("unroll") for (int m = 0; m < 4; ++m) _Pragma("unroll") for (int n = 0; n < 2; ++n) \
;         asm volatile("v_mfma_f32_16x16x128_f8f6f4 %0, %1, %2, 0" : "=&v"(acc[ai][bj][m][n]) : "v"(Bt##8[n]), "v"(At##8[m])); __builtin_amdgcn_s_setprio(0); } while (0)
; template <class Epi, class Sched, bool F8 = false>
; DI void gemm_phase(LAS unsigned char* lds, const int K, const Sched& S, const Epi& E) {
;     ...
;         const bool has_next = S.next(ui + 1, nxt);
;         const char* nA = has_next ? S.a_base(nxt) : cA; const char* nB = has_next ? S.b_base(nxt) : cB;
;         for (int t = 0; t < nt; t += 2) {
;             const bool last = (t == nt - 2); const int sxe = (t == 0) ? sx : 0;
;             const char* a1 = cA + (size_t)(t + 1) * kstep;
;             const char* a2 = last ? nA : cA + (size_t)(t + 2) * kstep; const char* b2 = last ? nB : cB + (size_t)(t + 2) * kstep;
;             const char* a3 = a2 + kstep; const char* b3 = b2 + kstep;
;             PG8_LDB(B0, 0, 0); PG8_LDB(B1, 0, 1); PG8_SCHED; PG8_LDA(At, 0, 0); PG8_STAGE(PG8_SA(1, 1), a1, oA[1]);
;             if (last && has_next) S.a_off(nxt, tid, oA);
;             PG8_WAIT_VX(sxe); PG8_WAIT_L(0); PG8_BAR; if (F8 && t == 0) { PG8_MMA0(0, 0, At, B0); PG8_MMA0(0, 1, At, B1); } else { PG8_MMA(0, 0, At, B0); PG8_MMA(0, 1, At, B1); } PG8_BAR; PG8_SCHED;
;             PG8_LDA(At, 0, 1); PG8_STAGE(PG8_SB(0, 0), b2, voffB); PG8_STAGE(PG8_SB(0, 1), b2 + hstep, voffB); PG8_STAGE(PG8_SA(0, 0), a2, oA[0]);
;             PG8_WAIT_VX(sxe); PG8_WAIT_L(0); PG8_BAR; if (F8 && t == 0) { PG8_MMA0(1, 0, At, B0); PG8_MMA0(1, 1, At, B1); } else { PG8_MMA(1, 0, At, B0); PG8_MMA(1, 1, At, B1); } PG8_BAR; PG8_SCHED;
.LBB0_1042:
	s_ashr_i32 s53, s52, 31
	s_lshl_b64 s[8:9], s[52:53], 18
	s_add_u32 s54, s67, s8
	s_addc_u32 s55, s68, s9
	v_add_u32_e32 v190, s76, v188
	v_add_u32_e32 v191, s80, v188
	s_and_b64 s[8:9], s[40:41], exec
	ds_read_b128 v[6:9], v190
	ds_read_b128 v[10:13], v190 offset:1024
	ds_read_b128 v[14:17], v190 offset:2048
	ds_read_b128 v[18:21], v190 offset:3072
	ds_read_b128 v[22:25], v191
	ds_read_b128 v[26:29], v191 offset:1024
	ds_read_b128 v[30:33], v191 offset:2048
	ds_read_b128 v[34:37], v191 offset:3072
	s_cselect_b32 s17, s55, s59
	s_cselect_b32 s53, s54, s58
	s_ashr_i32 s51, s50, 31
	s_lshl_b64 s[8:9], s[50:51], 18
	s_add_u32 s56, s74, s8
	s_addc_u32 s57, s75, s9
	s_and_b64 s[8:9], s[40:41], exec
	v_mov_b64_e32 v[210:211], 0x10000
	s_cselect_b32 s51, s57, s61
	s_cselect_b32 vcc_lo, s56, s60
	v_lshl_add_u64 v[220:221], s[58:59], 0, v[170:171]
	s_add_i32 vcc_hi, s6, 0xc000
	v_lshl_add_u64 v[70:71], v[220:221], 0, s[24:25]
	s_mov_b32 m0, vcc_hi
	v_lshl_add_u64 v[244:245], s[58:59], 0, v[174:175]
	s_add_i32 s83, s6, 0xe000
	ds_read_b128 v[38:41], v189
	ds_read_b128 v[42:45], v189 offset:1024
	ds_read_b128 v[46:49], v189 offset:2048
	ds_read_b128 v[50:53], v189 offset:3072
	ds_read_b128 v[54:57], v189 offset:4096
	ds_read_b128 v[58:61], v189 offset:5120
	ds_read_b128 v[62:65], v189 offset:6144
	ds_read_b128 v[66:69], v189 offset:7168
	global_load_lds_dwordx4 v[70:71], off
	v_lshl_add_u64 v[70:71], v[244:245], 0, s[24:25]
	s_mov_b32 m0, s83
	s_nop 0
	global_load_lds_dwordx4 v[70:71], off
	s_waitcnt vmcnt(8)
	s_waitcnt lgkmcnt(0)
	s_barrier
	s_setprio 1
	s_waitcnt lgkmcnt(0)
	v_mfma_f32_16x16x128_f8f6f4 v[162:165], v[6:13], v[38:45], 0
	v_mfma_f32_16x16x128_f8f6f4 v[158:161], v[14:21], v[38:45], 0
	v_mfma_f32_16x16x128_f8f6f4 v[146:149], v[6:13], v[46:53], 0
	v_mfma_f32_16x16x128_f8f6f4 v[142:145], v[14:21], v[46:53], 0
	v_mfma_f32_16x16x128_f8f6f4 v[130:133], v[6:13], v[54:61], 0
	v_mfma_f32_16x16x128_f8f6f4 v[126:129], v[14:21], v[54:61], 0
	v_mfma_f32_16x16x128_f8f6f4 v[114:117], v[6:13], v[62:69], 0
	v_mfma_f32_16x16x128_f8f6f4 v[110:113], v[14:21], v[62:69], 0
	s_setprio 0
	s_setprio 1
	v_mfma_f32_16x16x128_f8f6f4 v[154:157], v[22:29], v[38:45], 0
	v_mfma_f32_16x16x128_f8f6f4 v[150:153], v[30:37], v[38:45], 0
	v_mfma_f32_16x16x128_f8f6f4 v[138:141], v[22:29], v[46:53], 0
	v_mfma_f32_16x16x128_f8f6f4 v[134:137], v[30:37], v[46:53], 0
	v_mfma_f32_16x16x128_f8f6f4 v[122:125], v[22:29], v[54:61], 0
	v_mfma_f32_16x16x128_f8f6f4 v[118:121], v[30:37], v[54:61], 0
	v_mfma_f32_16x16x128_f8f6f4 v[98:101], v[22:29], v[62:69], 0
	v_mfma_f32_16x16x128_f8f6f4 v[90:93], v[30:37], v[62:69], 0
	s_setprio 0
	s_barrier
	v_lshl_add_u64 v[180:181], s[60:61], 0, v[2:3]
	s_mov_b32 m0, s78
	v_lshl_add_u64 v[46:47], v[180:181], 0, s[28:29]
	v_lshl_add_u64 v[182:183], s[60:61], 0, v[166:167]
	s_add_u32 s8, s60, 0x20100
	ds_read_b128 v[38:41], v189 offset:16384
	ds_read_b128 v[42:45], v189 offset:17408
	ds_read_b128 v[54:57], v189 offset:18432
	ds_read_b128 v[58:61], v189 offset:19456
	ds_read_b128 v[192:195], v189 offset:20480
	ds_read_b128 v[196:199], v189 offset:21504
	ds_read_b128 v[212:215], v189 offset:22528
	ds_read_b128 v[216:219], v189 offset:23552
	global_load_lds_dwordx4 v[46:47], off
	v_lshl_add_u64 v[46:47], v[182:183], 0, s[28:29]
	s_mov_b32 m0, s79
	s_addc_u32 s9, s61, 0
	global_load_lds_dwordx4 v[46:47], off
	v_lshl_add_u64 v[46:47], s[8:9], 0, v[2:3]
	s_mov_b32 m0, s81
	v_lshl_add_u64 v[184:185], s[58:59], 0, v[168:169]
	global_load_lds_dwordx4 v[46:47], off
	v_lshl_add_u64 v[46:47], s[8:9], 0, v[166:167]
	s_mov_b32 m0, s82
	v_lshl_add_u64 v[186:187], s[58:59], 0, v[172:173]
	global_load_lds_dwordx4 v[46:47], off
	v_lshl_add_u64 v[46:47], v[184:185], 0, s[28:29]
	s_mov_b32 m0, s6
	s_nop 0
	global_load_lds_dwordx4 v[46:47], off
	v_lshl_add_u64 v[46:47], v[186:187], 0, s[28:29]
	s_mov_b32 m0, s84
	s_nop 0
	global_load_lds_dwordx4 v[46:47], off
	s_waitcnt vmcnt(8)
	s_waitcnt lgkmcnt(0)
	s_barrier
	s_setprio 1
	s_waitcnt lgkmcnt(0)
	v_mfma_f32_16x16x128_f8f6f4 v[106:109], v[6:13], v[38:45], 0
	v_mfma_f32_16x16x128_f8f6f4 v[102:105], v[14:21], v[38:45], 0
	v_mfma_f32_16x16x128_f8f6f4 v[82:85], v[6:13], v[54:61], 0
	v_mfma_f32_16x16x128_f8f6f4 v[78:81], v[14:21], v[54:61], 0
	v_mfma_f32_16x16x128_f8f6f4 v[66:69], v[6:13], v[192:199], 0
	v_mfma_f32_16x16x128_f8f6f4 v[62:65], v[14:21], v[192:199], 0
	v_mfma_f32_16x16x128_f8f6f4 v[50:53], v[6:13], v[212:219], 0
	v_mfma_f32_16x16x128_f8f6f4 v[46:49], v[14:21], v[212:219], 0
	s_setprio 0
	s_setprio 1
	v_mfma_f32_16x16x128_f8f6f4 v[94:97], v[22:29], v[38:45], 0
	v_mfma_f32_16x16x128_f8f6f4 v[86:89], v[30:37], v[38:45], 0
	v_mfma_f32_16x16x128_f8f6f4 v[74:77], v[22:29], v[54:61], 0
	v_mfma_f32_16x16x128_f8f6f4 v[70:73], v[30:37], v[54:61], 0
	v_mfma_f32_16x16x128_f8f6f4 v[58:61], v[22:29], v[192:199], 0
	v_mfma_f32_16x16x128_f8f6f4 v[54:57], v[30:37], v[192:199], 0
	v_mfma_f32_16x16x128_f8f6f4 v[42:45], v[22:29], v[212:219], 0
	v_mfma_f32_16x16x128_f8f6f4 v[38:41], v[30:37], v[212:219], 0
	s_setprio 0
	s_barrier
; #define PG8_STAGE(bufoff, gbase, voff) do { _Pragma("unroll") for (int _i = 0; _i < 2; ++_i) \
;         __builtin_amdgcn_global_load_lds((const unsigned*)((const char*)(gbase) + (voff)[_i]), (LAS unsigned*)(lds + (bufoff) + ldsw + _i * 8192), 16, 0, 0); } while (0)
; #define PG8_LDA(dst, b, h) do { if constexpr (F8) { _Pragma("unroll") for (int m = 0; m < 4; ++m) dst##8[m] = PG8_LD8(lds + PG8_SA(b, h) + aoff + m * 2048); } else { \
;         _Pragma("unroll") for (int m = 0; m < 4; ++m) _Pragma("unroll") for (int k = 0; k < 2; ++k) dst[m][k] = *(const LAS bf16x8*)(lds + PG8_SA(b, h) + aoff + m * 2048 + k * 1024); } } while (0)
; #define PG8_LDB(dst, b, h) do { if constexpr (F8) { _Pragma("unroll") for (int n = 0; n < 2; ++n) dst##8[n] = PG8_LD8(lds + PG8_SB(b, h) + boff + n * 2048); } else { \
;         _Pragma("unroll") for (int n = 0; n < 2; ++n) _Pragma("unroll") for (int k = 0; k < 2; ++k) dst[n][k] = *(const LAS bf16x8*)(lds + PG8_SB(b, h) + boff + n * 2048 + k * 1024); } } while (0)
; #define PG8_WAIT_V(n) asm volatile("s_waitcnt vmcnt(" #n ")" ::: "memory")
; #define PG8_WAIT_L(n) asm volatile("s_waitcnt lgkmcnt(" #n ")" ::: "memory")
; #define PG8_BAR __builtin_amdgcn_s_barrier()
; #define PG8_SCHED __builtin_amdgcn_sched_barrier(0)
; template <class Epi, class Sched, bool F8 = false>
; DI void gemm_phase(LAS unsigned char* lds, const int K, const Sched& S, const Epi& E) {
;     ...
;             PG8_LDB(B0, 1, 0); PG8_LDB(B1, 1, 1); PG8_SCHED; PG8_LDA(At, 1, 0); PG8_STAGE(PG8_SA(0, 1), a2, oA[1]);
;             PG8_WAIT_V(8); PG8_WAIT_L(0); PG8_BAR; PG8_MMA(0, 0, At, B0); PG8_MMA(0, 1, At, B1); PG8_BAR; PG8_SCHED;
;             PG8_LDA(At, 1, 1); PG8_STAGE(PG8_SB(1, 0), b3, voffB); PG8_STAGE(PG8_SB(1, 1), b3 + hstep, voffB); PG8_STAGE(PG8_SA(1, 0), a3, oA[0]);
;             PG8_WAIT_V(8); PG8_WAIT_L(0); PG8_BAR; PG8_MMA(1, 0, At, B0); PG8_MMA(1, 1, At, B1); PG8_BAR; PG8_SCHED;
;         }
	v_add_u32_e32 v192, s89, v188
	v_add_u32_e32 v193, s94, v188
	ds_read_b128 v[22:25], v192
	ds_read_b128 v[26:29], v192 offset:1024
	ds_read_b128 v[30:33], v192 offset:2048
	ds_read_b128 v[34:37], v192 offset:3072
	ds_read_b128 v[6:9], v193
	ds_read_b128 v[10:13], v193 offset:1024
	ds_read_b128 v[14:17], v193 offset:2048
	ds_read_b128 v[18:21], v193 offset:3072
	s_mov_b32 m0, s85
	v_lshl_add_u64 v[220:221], v[220:221], 0, s[28:29]
	ds_read_b128 v[194:197], v189 offset:32768
	ds_read_b128 v[198:201], v189 offset:33792
	ds_read_b128 v[212:215], v189 offset:34816
	ds_read_b128 v[216:219], v189 offset:35840
	ds_read_b128 v[226:229], v189 offset:36864
	ds_read_b128 v[230:233], v189 offset:37888
	ds_read_b128 v[236:239], v189 offset:38912
	ds_read_b128 v[240:243], v189 offset:39936
	global_load_lds_dwordx4 v[220:221], off
	v_lshl_add_u64 v[220:221], v[244:245], 0, s[28:29]
	s_mov_b32 m0, s86
	s_nop 0
	global_load_lds_dwordx4 v[220:221], off
	s_waitcnt vmcnt(8)
	s_waitcnt lgkmcnt(0)
	s_barrier
	s_setprio 1
	s_waitcnt lgkmcnt(0)
	v_mfma_f32_16x16x128_f8f6f4 v[162:165], v[22:29], v[194:201], v[162:165]
	v_mfma_f32_16x16x128_f8f6f4 v[158:161], v[30:37], v[194:201], v[158:161]
	v_mfma_f32_16x16x128_f8f6f4 v[146:149], v[22:29], v[212:219], v[146:149]
	v_mfma_f32_16x16x128_f8f6f4 v[142:145], v[30:37], v[212:219], v[142:145]
	v_mfma_f32_16x16x128_f8f6f4 v[130:133], v[22:29], v[226:233], v[130:133]
	v_mfma_f32_16x16x128_f8f6f4 v[126:129], v[30:37], v[226:233], v[126:129]
	v_mfma_f32_16x16x128_f8f6f4 v[114:117], v[22:29], v[236:243], v[114:117]
	v_mfma_f32_16x16x128_f8f6f4 v[110:113], v[30:37], v[236:243], v[110:113]
	s_setprio 0
	s_setprio 1
	v_mfma_f32_16x16x128_f8f6f4 v[154:157], v[6:13], v[194:201], v[154:157]
	v_mfma_f32_16x16x128_f8f6f4 v[150:153], v[14:21], v[194:201], v[150:153]
	v_mfma_f32_16x16x128_f8f6f4 v[138:141], v[6:13], v[212:219], v[138:141]
	v_mfma_f32_16x16x128_f8f6f4 v[134:137], v[14:21], v[212:219], v[134:137]
	v_mfma_f32_16x16x128_f8f6f4 v[122:125], v[6:13], v[226:233], v[122:125]
	v_mfma_f32_16x16x128_f8f6f4 v[118:121], v[14:21], v[226:233], v[118:121]
	v_mfma_f32_16x16x128_f8f6f4 v[98:101], v[6:13], v[236:243], v[98:101]
	v_mfma_f32_16x16x128_f8f6f4 v[90:93], v[14:21], v[236:243], v[90:93]
	s_setprio 0
	s_barrier
	s_mov_b32 m0, s90
	v_lshl_add_u64 v[180:181], v[180:181], 0, s[26:27]
	s_add_u32 s8, s60, 0x20180
	ds_read_b128 v[194:197], v189 offset:49152
	ds_read_b128 v[198:201], v189 offset:50176
	ds_read_b128 v[212:215], v189 offset:51200
	ds_read_b128 v[216:219], v189 offset:52224
	ds_read_b128 v[226:229], v189 offset:53248
	ds_read_b128 v[230:233], v189 offset:54272
	ds_read_b128 v[236:239], v189 offset:55296
	ds_read_b128 v[240:243], v189 offset:56320
	global_load_lds_dwordx4 v[180:181], off
	v_lshl_add_u64 v[180:181], v[182:183], 0, s[26:27]
	s_mov_b32 m0, s91
	s_addc_u32 s9, s61, 0
	global_load_lds_dwordx4 v[180:181], off
	v_lshl_add_u64 v[180:181], s[8:9], 0, v[2:3]
	s_mov_b32 m0, s95
	s_nop 0
	global_load_lds_dwordx4 v[180:181], off
	v_lshl_add_u64 v[180:181], s[8:9], 0, v[166:167]
	s_mov_b32 m0, s96
	s_nop 0
	global_load_lds_dwordx4 v[180:181], off
	v_lshl_add_u64 v[180:181], v[184:185], 0, s[26:27]
	s_mov_b32 m0, s92
	s_nop 0
	global_load_lds_dwordx4 v[180:181], off
	v_lshl_add_u64 v[180:181], v[186:187], 0, s[26:27]
	s_mov_b32 m0, s93
	s_nop 0
	global_load_lds_dwordx4 v[180:181], off
	s_waitcnt vmcnt(8)
	s_waitcnt lgkmcnt(0)
	s_barrier
	s_setprio 1
	s_waitcnt lgkmcnt(0)
	v_mfma_f32_16x16x128_f8f6f4 v[106:109], v[22:29], v[194:201], v[106:109]
	v_mfma_f32_16x16x128_f8f6f4 v[102:105], v[30:37], v[194:201], v[102:105]
	v_mfma_f32_16x16x128_f8f6f4 v[82:85], v[22:29], v[212:219], v[82:85]
	v_mfma_f32_16x16x128_f8f6f4 v[78:81], v[30:37], v[212:219], v[78:81]
	v_mfma_f32_16x16x128_f8f6f4 v[66:69], v[22:29], v[226:233], v[66:69]
	v_mfma_f32_16x16x128_f8f6f4 v[62:65], v[30:37], v[226:233], v[62:65]
	v_mfma_f32_16x16x128_f8f6f4 v[50:53], v[22:29], v[236:243], v[50:53]
	v_mfma_f32_16x16x128_f8f6f4 v[46:49], v[30:37], v[236:243], v[46:49]
	s_setprio 0
	s_setprio 1
	v_mfma_f32_16x16x128_f8f6f4 v[94:97], v[6:13], v[194:201], v[94:97]
	v_mfma_f32_16x16x128_f8f6f4 v[86:89], v[14:21], v[194:201], v[86:89]
	v_mfma_f32_16x16x128_f8f6f4 v[74:77], v[6:13], v[212:219], v[74:77]
	v_mfma_f32_16x16x128_f8f6f4 v[70:73], v[14:21], v[212:219], v[70:73]
	v_mfma_f32_16x16x128_f8f6f4 v[58:61], v[6:13], v[226:233], v[58:61]
	v_mfma_f32_16x16x128_f8f6f4 v[54:57], v[14:21], v[226:233], v[54:57]
	v_mfma_f32_16x16x128_f8f6f4 v[42:45], v[6:13], v[236:243], v[42:45]
	v_mfma_f32_16x16x128_f8f6f4 v[38:41], v[14:21], v[236:243], v[38:41]
	s_setprio 0
	s_barrier
	s_add_u32 s7, s60, 0x200
	s_addc_u32 s8, s61, 0
	s_mov_b32 s9, 0
	.p2alignl 6, 3212836864

; #define PG8_STAGE(bufoff, gbase, voff) do { _Pragma("unroll") for (int _i = 0; _i < 2; ++_i) \
;         __builtin_amdgcn_global_load_lds((const unsigned*)((const char*)(gbase) + (voff)[_i]), (LAS unsigned*)(lds + (bufoff) + ldsw + _i * 8192), 16, 0, 0); } while (0)
; #define PG8_LDA(dst, b, h) do { if constexpr (F8) { _Pragma("unroll") for (int m = 0; m < 4; ++m) dst##8[m] = PG8_LD8(lds + PG8_SA(b, h) + aoff + m * 2048); } else { \
;         _Pragma("unroll") for (int m = 0; m < 4; ++m) _Pragma("unroll") for (int k = 0; k < 2; ++k) dst[m][k] = *(const LAS bf16x8*)(lds + PG8_SA(b, h) + aoff + m * 2048 + k * 1024); } } while (0)
; #define PG8_LDB(dst, b, h) do { if constexpr (F8) { _Pragma("unroll") for (int n = 0; n < 2; ++n) dst##8[n] = PG8_LD8(lds + PG8_SB(b, h) + boff + n * 2048); } else { \
;         _Pragma("unroll") for (int n = 0; n < 2; ++n) _Pragma("unroll") for (int k = 0; k < 2; ++k) dst[n][k] = *(const LAS bf16x8*)(lds + PG8_SB(b, h) + boff + n * 2048 + k * 1024); } } while (0)
; #define PG8_WAIT_L(n) asm volatile("s_waitcnt lgkmcnt(" #n ")" ::: "memory")
; #define PG8_BAR __builtin_amdgcn_s_barrier()
; template <class Epi, class Sched, bool F8 = false>
; DI void gemm_phase(LAS unsigned char* lds, const int K, const Sched& S, const Epi& E) {
;     ...
;             const bool last = (t == nt - 2); const int sxe = (t == 0) ? sx : 0;
;             const char* a1 = cA + (size_t)(t + 1) * kstep;
;             const char* a2 = last ? nA : cA + (size_t)(t + 2) * kstep; const char* b2 = last ? nB : cB + (size_t)(t + 2) * kstep;
;             const char* a3 = a2 + kstep; const char* b3 = b2 + kstep;
;             PG8_LDB(B0, 0, 0); PG8_LDB(B1, 0, 1); PG8_SCHED; PG8_LDA(At, 0, 0); PG8_STAGE(PG8_SA(1, 1), a1, oA[1]);
;             if (last && has_next) S.a_off(nxt, tid, oA);
;             PG8_WAIT_VX(sxe); PG8_WAIT_L(0); PG8_BAR; if (F8 && t == 0) { PG8_MMA0(0, 0, At, B0); PG8_MMA0(0, 1, At, B1); } else { PG8_MMA(0, 0, At, B0); PG8_MMA(0, 1, At, B1); } PG8_BAR; PG8_SCHED;
;             PG8_LDA(At, 0, 1); PG8_STAGE(PG8_SB(0, 0), b2, voffB); PG8_STAGE(PG8_SB(0, 1), b2 + hstep, voffB); PG8_STAGE(PG8_SA(0, 0), a2, oA[0]);
;             PG8_WAIT_VX(sxe); PG8_WAIT_L(0); PG8_BAR; if (F8 && t == 0) { PG8_MMA0(1, 0, At, B0); PG8_MMA0(1, 1, At, B1); } else { PG8_MMA(1, 0, At, B0); PG8_MMA(1, 1, At, B1); } PG8_BAR; PG8_SCHED;
.LBB0_1362:
	s_waitcnt vmcnt(8)
	s_add_u32 s10, s60, 0x80
	s_waitcnt lgkmcnt(0)
	s_addc_u32 s11, s61, 0
	s_and_b64 s[8:9], s[62:63], exec
	v_mov_b32_e32 v217, v4
	v_mov_b32_e32 v221, v4
	s_cselect_b32 vcc_hi, s43, s11
	s_cselect_b32 vcc_lo, s42, s10
	s_cselect_b32 s63, s59, s7
	s_cselect_b32 s62, s58, s6
	s_barrier
	s_setprio 1
	s_waitcnt lgkmcnt(0)
	v_mfma_f32_16x16x128_f8f6f4 v[190:193], v[30:37], v[62:69], v[190:193]
	v_mfma_f32_16x16x128_f8f6f4 v[182:185], v[22:29], v[62:69], v[182:185]
	v_mfma_f32_16x16x128_f8f6f4 v[174:177], v[30:37], v[54:61], v[174:177]
	v_mfma_f32_16x16x128_f8f6f4 v[166:169], v[22:29], v[54:61], v[166:169]
	v_mfma_f32_16x16x128_f8f6f4 v[158:161], v[30:37], v[46:53], v[158:161]
	v_mfma_f32_16x16x128_f8f6f4 v[150:153], v[22:29], v[46:53], v[150:153]
	v_mfma_f32_16x16x128_f8f6f4 v[142:145], v[30:37], v[38:45], v[142:145]
	v_mfma_f32_16x16x128_f8f6f4 v[134:137], v[22:29], v[38:45], v[134:137]
	s_setprio 0
	s_setprio 1
	v_mfma_f32_16x16x128_f8f6f4 v[194:197], v[14:21], v[62:69], v[194:197]
	v_mfma_f32_16x16x128_f8f6f4 v[186:189], v[6:13], v[62:69], v[186:189]
	v_mfma_f32_16x16x128_f8f6f4 v[178:181], v[14:21], v[54:61], v[178:181]
	v_mfma_f32_16x16x128_f8f6f4 v[170:173], v[6:13], v[54:61], v[170:173]
	v_mfma_f32_16x16x128_f8f6f4 v[162:165], v[14:21], v[46:53], v[162:165]
	v_mfma_f32_16x16x128_f8f6f4 v[154:157], v[6:13], v[46:53], v[154:157]
	v_mfma_f32_16x16x128_f8f6f4 v[146:149], v[14:21], v[38:45], v[146:149]
	v_mfma_f32_16x16x128_f8f6f4 v[138:141], v[6:13], v[38:45], v[138:141]
	s_setprio 0
	s_barrier
	s_mov_b32 m0, s0
	v_lshl_add_u64 v[38:39], s[62:63], 0, v[212:213]
	s_add_u32 s8, s62, 0x20000
	ds_read_b128 v[46:49], v240 offset:16384
	ds_read_b128 v[50:53], v240 offset:17408
	ds_read_b128 v[54:57], v240 offset:18432
	ds_read_b128 v[58:61], v240 offset:19456
	ds_read_b128 v[62:65], v240 offset:20480
	ds_read_b128 v[66:69], v240 offset:21504
	ds_read_b128 v[226:229], v240 offset:22528
	ds_read_b128 v[230:233], v240 offset:23552
	global_load_lds_dwordx4 v[38:39], off
	v_lshl_add_u64 v[40:41], s[62:63], 0, v[2:3]
	s_mov_b32 m0, s97
	s_addc_u32 s9, s63, 0
	global_load_lds_dwordx4 v[40:41], off
	v_lshl_add_u64 v[42:43], s[8:9], 0, v[212:213]
	s_mov_b32 m0, s30
	v_mov_b32_e32 v215, v4
	global_load_lds_dwordx4 v[42:43], off
	v_lshl_add_u64 v[42:43], s[8:9], 0, v[2:3]
	s_mov_b32 m0, s31
	v_mov_b32_e32 v219, v4
	global_load_lds_dwordx4 v[42:43], off
	s_mov_b32 m0, s5
	v_lshl_add_u64 v[44:45], vcc, 0, v[214:215]
	global_load_lds_dwordx4 v214, vcc
	s_mov_b32 m0, s95
	v_lshl_add_u64 v[42:43], vcc, 0, v[218:219]
	global_load_lds_dwordx4 v218, vcc
	s_waitcnt vmcnt(8)
	s_waitcnt lgkmcnt(0)
	s_barrier
	s_setprio 1
	s_waitcnt lgkmcnt(0)
	v_mfma_f32_16x16x128_f8f6f4 v[126:129], v[30:37], v[46:53], v[126:129]
	v_mfma_f32_16x16x128_f8f6f4 v[118:121], v[22:29], v[46:53], v[118:121]
	v_mfma_f32_16x16x128_f8f6f4 v[110:113], v[30:37], v[54:61], v[110:113]
	v_mfma_f32_16x16x128_f8f6f4 v[102:105], v[22:29], v[54:61], v[102:105]
	v_mfma_f32_16x16x128_f8f6f4 v[94:97], v[30:37], v[62:69], v[94:97]
	v_mfma_f32_16x16x128_f8f6f4 v[86:89], v[22:29], v[62:69], v[86:89]
	v_mfma_f32_16x16x128_f8f6f4 v[78:81], v[30:37], v[226:233], v[78:81]
	v_mfma_f32_16x16x128_f8f6f4 v[70:73], v[22:29], v[226:233], v[70:73]
	s_setprio 0
	s_setprio 1
	v_mfma_f32_16x16x128_f8f6f4 v[130:133], v[14:21], v[46:53], v[130:133]
	v_mfma_f32_16x16x128_f8f6f4 v[122:125], v[6:13], v[46:53], v[122:125]
	v_mfma_f32_16x16x128_f8f6f4 v[114:117], v[14:21], v[54:61], v[114:117]
	v_mfma_f32_16x16x128_f8f6f4 v[106:109], v[6:13], v[54:61], v[106:109]
	v_mfma_f32_16x16x128_f8f6f4 v[98:101], v[14:21], v[62:69], v[98:101]
	v_mfma_f32_16x16x128_f8f6f4 v[90:93], v[6:13], v[62:69], v[90:93]
	v_mfma_f32_16x16x128_f8f6f4 v[82:85], v[14:21], v[226:233], v[82:85]
	v_mfma_f32_16x16x128_f8f6f4 v[74:77], v[6:13], v[226:233], v[74:77]
	s_setprio 0
	s_barrier
; #define PG8_STAGE(bufoff, gbase, voff) do { _Pragma("unroll") for (int _i = 0; _i < 2; ++_i) \
;         __builtin_amdgcn_global_load_lds((const unsigned*)((const char*)(gbase) + (voff)[_i]), (LAS unsigned*)(lds + (bufoff) + ldsw + _i * 8192), 16, 0, 0); } while (0)
; #define PG8_LDA(dst, b, h) do { if constexpr (F8) { _Pragma("unroll") for (int m = 0; m < 4; ++m) dst##8[m] = PG8_LD8(lds + PG8_SA(b, h) + aoff + m * 2048); } else { \
;         _Pragma("unroll") for (int m = 0; m < 4; ++m) _Pragma("unroll") for (int k = 0; k < 2; ++k) dst[m][k] = *(const LAS bf16x8*)(lds + PG8_SA(b, h) + aoff + m * 2048 + k * 1024); } } while (0)
; #define PG8_LDB(dst, b, h) do { if constexpr (F8) { _Pragma("unroll") for (int n = 0; n < 2; ++n) dst##8[n] = PG8_LD8(lds + PG8_SB(b, h) + boff + n * 2048); } else { \
;         _Pragma("unroll") for (int n = 0; n < 2; ++n) _Pragma("unroll") for (int k = 0; k < 2; ++k) dst[n][k] = *(const LAS bf16x8*)(lds + PG8_SB(b, h) + boff + n * 2048 + k * 1024); } } while (0)
; #define PG8_WAIT_V(n) asm volatile("s_waitcnt vmcnt(" #n ")" ::: "memory")
; #define PG8_WAIT_L(n) asm volatile("s_waitcnt lgkmcnt(" #n ")" ::: "memory")
; #define PG8_BAR __builtin_amdgcn_s_barrier()
; #define PG8_SCHED __builtin_amdgcn_sched_barrier(0)
; template <class Epi, class Sched, bool F8 = false>
; DI void gemm_phase(LAS unsigned char* lds, const int K, const Sched& S, const Epi& E) {
;     ...
;             PG8_LDB(B0, 1, 0); PG8_LDB(B1, 1, 1); PG8_SCHED; PG8_LDA(At, 1, 0); PG8_STAGE(PG8_SA(0, 1), a2, oA[1]);
;             PG8_WAIT_V(8); PG8_WAIT_L(0); PG8_BAR; PG8_MMA(0, 0, At, B0); PG8_MMA(0, 1, At, B1); PG8_BAR; PG8_SCHED;
;             PG8_LDA(At, 1, 1); PG8_STAGE(PG8_SB(1, 0), b3, voffB); PG8_STAGE(PG8_SB(1, 1), b3 + hstep, voffB); PG8_STAGE(PG8_SA(1, 0), a3, oA[0]);
;             PG8_WAIT_V(8); PG8_WAIT_L(0); PG8_BAR; PG8_MMA(1, 0, At, B0); PG8_MMA(1, 1, At, B1); PG8_BAR; PG8_SCHED;
;         }
	ds_read_b128 v[14:17], v242
	ds_read_b128 v[18:21], v242 offset:1024
	ds_read_b128 v[22:25], v242 offset:2048
	ds_read_b128 v[26:29], v242 offset:3072
	ds_read_b128 v[6:9], v243
	ds_read_b128 v[10:13], v243 offset:1024
	ds_read_b128 v[30:33], v243 offset:2048
	ds_read_b128 v[34:37], v243 offset:3072
	s_mov_b32 m0, s44
	v_lshl_add_u64 v[198:199], vcc, 0, v[216:217]
	ds_read_b128 v[46:49], v240 offset:32768
	ds_read_b128 v[50:53], v240 offset:33792
	ds_read_b128 v[54:57], v240 offset:34816
	ds_read_b128 v[58:61], v240 offset:35840
	ds_read_b128 v[62:65], v240 offset:36864
	ds_read_b128 v[66:69], v240 offset:37888
	ds_read_b128 v[226:229], v240 offset:38912
	ds_read_b128 v[230:233], v240 offset:39936
	global_load_lds_dwordx4 v[198:199], off
	v_lshl_add_u64 v[198:199], vcc, 0, v[220:221]
	s_mov_b32 m0, s45
	s_nop 0
	global_load_lds_dwordx4 v[198:199], off
	s_waitcnt vmcnt(8)
	s_waitcnt lgkmcnt(0)
	s_barrier
	s_setprio 1
	s_waitcnt lgkmcnt(0)
	v_mfma_f32_16x16x128_f8f6f4 v[190:193], v[14:21], v[46:53], v[190:193]
	v_mfma_f32_16x16x128_f8f6f4 v[182:185], v[22:29], v[46:53], v[182:185]
	v_mfma_f32_16x16x128_f8f6f4 v[174:177], v[14:21], v[54:61], v[174:177]
	v_mfma_f32_16x16x128_f8f6f4 v[166:169], v[22:29], v[54:61], v[166:169]
	v_mfma_f32_16x16x128_f8f6f4 v[158:161], v[14:21], v[62:69], v[158:161]
	v_mfma_f32_16x16x128_f8f6f4 v[150:153], v[22:29], v[62:69], v[150:153]
	v_mfma_f32_16x16x128_f8f6f4 v[142:145], v[14:21], v[226:233], v[142:145]
	v_mfma_f32_16x16x128_f8f6f4 v[134:137], v[22:29], v[226:233], v[134:137]
	s_setprio 0
	s_setprio 1
	v_mfma_f32_16x16x128_f8f6f4 v[194:197], v[6:13], v[46:53], v[194:197]
	v_mfma_f32_16x16x128_f8f6f4 v[186:189], v[30:37], v[46:53], v[186:189]
	v_mfma_f32_16x16x128_f8f6f4 v[178:181], v[6:13], v[54:61], v[178:181]
	v_mfma_f32_16x16x128_f8f6f4 v[170:173], v[30:37], v[54:61], v[170:173]
	v_mfma_f32_16x16x128_f8f6f4 v[162:165], v[6:13], v[62:69], v[162:165]
	v_mfma_f32_16x16x128_f8f6f4 v[154:157], v[30:37], v[62:69], v[154:157]
	v_mfma_f32_16x16x128_f8f6f4 v[146:149], v[6:13], v[226:233], v[146:149]
	v_mfma_f32_16x16x128_f8f6f4 v[138:141], v[30:37], v[226:233], v[138:141]
	s_setprio 0
	s_barrier
	s_mov_b32 m0, s83
	v_lshl_add_u64 v[38:39], v[38:39], 0, s[24:25]
	s_add_u32 s8, s62, 0x20080
	ds_read_b128 v[46:49], v240 offset:49152
	ds_read_b128 v[50:53], v240 offset:50176
	ds_read_b128 v[54:57], v240 offset:51200
	ds_read_b128 v[58:61], v240 offset:52224
	ds_read_b128 v[62:65], v240 offset:53248
	ds_read_b128 v[66:69], v240 offset:54272
	ds_read_b128 v[226:229], v240 offset:55296
	ds_read_b128 v[230:233], v240 offset:56320
	global_load_lds_dwordx4 v[38:39], off
	v_lshl_add_u64 v[38:39], v[40:41], 0, s[24:25]
	s_mov_b32 m0, s82
	s_addc_u32 s9, s63, 0
	global_load_lds_dwordx4 v[38:39], off
	v_lshl_add_u64 v[38:39], s[8:9], 0, v[212:213]
	s_mov_b32 m0, s88
	s_nop 0
	global_load_lds_dwordx4 v[38:39], off
	v_lshl_add_u64 v[38:39], s[8:9], 0, v[2:3]
	s_mov_b32 m0, s87
	s_nop 0
	global_load_lds_dwordx4 v[38:39], off
	v_lshl_add_u64 v[38:39], v[44:45], 0, s[24:25]
	s_mov_b32 m0, s84
	s_nop 0
	global_load_lds_dwordx4 v[38:39], off
	v_lshl_add_u64 v[38:39], v[42:43], 0, s[24:25]
	s_mov_b32 m0, s85
	s_nop 0
	global_load_lds_dwordx4 v[38:39], off
	s_waitcnt vmcnt(8)
	s_waitcnt lgkmcnt(0)
	s_barrier
	s_setprio 1
	s_waitcnt lgkmcnt(0)
	v_mfma_f32_16x16x128_f8f6f4 v[126:129], v[14:21], v[46:53], v[126:129]
	v_mfma_f32_16x16x128_f8f6f4 v[118:121], v[22:29], v[46:53], v[118:121]
	v_mfma_f32_16x16x128_f8f6f4 v[110:113], v[14:21], v[54:61], v[110:113]
	v_mfma_f32_16x16x128_f8f6f4 v[102:105], v[22:29], v[54:61], v[102:105]
	v_mfma_f32_16x16x128_f8f6f4 v[94:97], v[14:21], v[62:69], v[94:97]
	v_mfma_f32_16x16x128_f8f6f4 v[86:89], v[22:29], v[62:69], v[86:89]
	v_mfma_f32_16x16x128_f8f6f4 v[78:81], v[14:21], v[226:233], v[78:81]
	v_mfma_f32_16x16x128_f8f6f4 v[70:73], v[22:29], v[226:233], v[70:73]
	s_setprio 0
	s_setprio 1
	v_mfma_f32_16x16x128_f8f6f4 v[130:133], v[6:13], v[46:53], v[130:133]
	v_mfma_f32_16x16x128_f8f6f4 v[122:125], v[30:37], v[46:53], v[122:125]
	v_mfma_f32_16x16x128_f8f6f4 v[114:117], v[6:13], v[54:61], v[114:117]
	v_mfma_f32_16x16x128_f8f6f4 v[106:109], v[30:37], v[54:61], v[106:109]
	v_mfma_f32_16x16x128_f8f6f4 v[98:101], v[6:13], v[62:69], v[98:101]
	v_mfma_f32_16x16x128_f8f6f4 v[90:93], v[30:37], v[62:69], v[90:93]
	v_mfma_f32_16x16x128_f8f6f4 v[82:85], v[6:13], v[226:233], v[82:85]
	v_mfma_f32_16x16x128_f8f6f4 v[74:77], v[30:37], v[226:233], v[74:77]
	s_setprio 0
	s_barrier
	s_add_i32 s67, s67, 2
	s_add_u32 s6, s6, 0x100
	s_addc_u32 s7, s7, 0
	s_add_u32 s60, s60, 0x100
	s_addc_u32 s61, s61, 0
	s_cmp_gt_u32 s67, 5
	s_cbranch_scc1 .LBB0_1365
	.p2alignl 6, 3212836864

; #define PG8_STAGE(bufoff, gbase, voff) do { _Pragma("unroll") for (int _i = 0; _i < 2; ++_i) \
;         __builtin_amdgcn_global_load_lds((const unsigned*)((const char*)(gbase) + (voff)[_i]), (LAS unsigned*)(lds + (bufoff) + ldsw + _i * 8192), 16, 0, 0); } while (0)
; #define PG8_LDA(dst, b, h) do { if constexpr (F8) { _Pragma("unroll") for (int m = 0; m < 4; ++m) dst##8[m] = PG8_LD8(lds + PG8_SA(b, h) + aoff + m * 2048); } else { \
;         _Pragma("unroll") for (int m = 0; m < 4; ++m) _Pragma("unroll") for (int k = 0; k < 2; ++k) dst[m][k] = *(const LAS bf16x8*)(lds + PG8_SA(b, h) + aoff + m * 2048 + k * 1024); } } while (0)
; #define PG8_MMA0(ai, bj, At, Bt) do { __builtin_amdgcn_s_setprio(1); _Pragma("unroll") for (int m = 0; m < 4; ++m) _Pragma("unroll") for (int n = 0; n < 2; ++n) \
;         asm volatile("v_mfma_f32_16x16x128_f8f6f4 %0, %1, %2, 0" : "=&v"(acc[ai][bj][m][n]) : "v"(Bt##8[n]), "v"(At##8[m])); __builtin_amdgcn_s_setprio(0); } while (0)
; template <class Epi, class Sched, bool F8 = false>
; DI void gemm_phase(LAS unsigned char* lds, const int K, const Sched& S, const Epi& E) {
;     ...
;         const bool has_next = S.next(ui + 1, nxt);
;         const char* nA = has_next ? S.a_base(nxt) : cA; const char* nB = has_next ? S.b_base(nxt) : cB;
;         for (int t = 0; t < nt; t += 2) {
;             const bool last = (t == nt - 2); const int sxe = (t == 0) ? sx : 0;
;             const char* a1 = cA + (size_t)(t + 1) * kstep;
;             const char* a2 = last ? nA : cA + (size_t)(t + 2) * kstep; const char* b2 = last ? nB : cB + (size_t)(t + 2) * kstep;
;             const char* a3 = a2 + kstep; const char* b3 = b2 + kstep;
;             PG8_LDB(B0, 0, 0); PG8_LDB(B1, 0, 1); PG8_SCHED; PG8_LDA(At, 0, 0); PG8_STAGE(PG8_SA(1, 1), a1, oA[1]);
;             if (last && has_next) S.a_off(nxt, tid, oA);
;             PG8_WAIT_VX(sxe); PG8_WAIT_L(0); PG8_BAR; if (F8 && t == 0) { PG8_MMA0(0, 0, At, B0); PG8_MMA0(0, 1, At, B1); } else { PG8_MMA(0, 0, At, B0); PG8_MMA(0, 1, At, B1); } PG8_BAR; PG8_SCHED;
;             PG8_LDA(At, 0, 1); PG8_STAGE(PG8_SB(0, 0), b2, voffB); PG8_STAGE(PG8_SB(0, 1), b2 + hstep, voffB); PG8_STAGE(PG8_SA(0, 0), a2, oA[0]);
;             PG8_WAIT_VX(sxe); PG8_WAIT_L(0); PG8_BAR; if (F8 && t == 0) { PG8_MMA0(1, 0, At, B0); PG8_MMA0(1, 1, At, B1); } else { PG8_MMA(1, 0, At, B0); PG8_MMA(1, 1, At, B1); } PG8_BAR; PG8_SCHED;
.LBB0_1640:
	v_add_u32_e32 v188, s82, v177
	v_add_u32_e32 v189, s85, v177
	ds_read_b128 v[6:9], v188
	s_nop 0
	ds_read_b128 v[10:13], v188 offset:1024
	ds_read_b128 v[14:17], v188 offset:2048
	ds_read_b128 v[18:21], v188 offset:3072
	ds_read_b128 v[22:25], v189
	ds_read_b128 v[26:29], v189 offset:1024
	ds_read_b128 v[30:33], v189 offset:2048
	ds_read_b128 v[34:37], v189 offset:3072
	s_ashr_i32 s17, s16, 31
	s_lshl_b64 s[0:1], s[16:17], 18
	s_add_u32 s0, s61, s0
	s_addc_u32 s1, s75, s1
	s_and_b64 s[6:7], s[46:47], exec
	s_cselect_b32 s17, s1, s49
	s_cselect_b32 s43, s0, s48
	v_mov_b32_e32 v171, v4
	v_lshl_add_u64 v[200:201], s[48:49], 0, v[170:171]
	s_add_i32 s45, s88, 0xc000
	v_mov_b32_e32 v175, v4
	v_lshl_add_u64 v[70:71], v[200:201], 0, s[24:25]
	s_mov_b32 m0, s45
	v_lshl_add_u64 v[220:221], s[48:49], 0, v[174:175]
	s_add_i32 s54, s88, 0xe000
	ds_read_b128 v[38:41], v179
	ds_read_b128 v[42:45], v179 offset:1024
	ds_read_b128 v[46:49], v179 offset:2048
	ds_read_b128 v[50:53], v179 offset:3072
	ds_read_b128 v[54:57], v179 offset:4096
	ds_read_b128 v[58:61], v179 offset:5120
	ds_read_b128 v[62:65], v179 offset:6144
	ds_read_b128 v[66:69], v179 offset:7168
	global_load_lds_dwordx4 v[70:71], off
	v_lshl_add_u64 v[70:71], v[220:221], 0, s[24:25]
	s_mov_b32 m0, s54
	s_nop 0
	global_load_lds_dwordx4 v[70:71], off
	s_waitcnt vmcnt(8)
	s_waitcnt lgkmcnt(0)
	s_barrier
	s_setprio 1
	s_waitcnt lgkmcnt(0)
	v_mfma_f32_16x16x128_f8f6f4 v[162:165], v[6:13], v[38:45], 0
	v_mfma_f32_16x16x128_f8f6f4 v[158:161], v[14:21], v[38:45], 0
	v_mfma_f32_16x16x128_f8f6f4 v[146:149], v[6:13], v[46:53], 0
	v_mfma_f32_16x16x128_f8f6f4 v[142:145], v[14:21], v[46:53], 0
	v_mfma_f32_16x16x128_f8f6f4 v[130:133], v[6:13], v[54:61], 0
	v_mfma_f32_16x16x128_f8f6f4 v[126:129], v[14:21], v[54:61], 0
	v_mfma_f32_16x16x128_f8f6f4 v[106:109], v[6:13], v[62:69], 0
	v_mfma_f32_16x16x128_f8f6f4 v[98:101], v[14:21], v[62:69], 0
	s_setprio 0
	s_setprio 1
	v_mfma_f32_16x16x128_f8f6f4 v[154:157], v[22:29], v[38:45], 0
	v_mfma_f32_16x16x128_f8f6f4 v[150:153], v[30:37], v[38:45], 0
	v_mfma_f32_16x16x128_f8f6f4 v[138:141], v[22:29], v[46:53], 0
	v_mfma_f32_16x16x128_f8f6f4 v[134:137], v[30:37], v[46:53], 0
	v_mfma_f32_16x16x128_f8f6f4 v[122:125], v[22:29], v[54:61], 0
	v_mfma_f32_16x16x128_f8f6f4 v[118:121], v[30:37], v[54:61], 0
	v_mfma_f32_16x16x128_f8f6f4 v[90:93], v[22:29], v[62:69], 0
	v_mfma_f32_16x16x128_f8f6f4 v[86:89], v[30:37], v[62:69], 0
	s_setprio 0
	s_barrier
	v_lshl_add_u64 v[180:181], s[50:51], 0, v[2:3]
	s_mov_b32 m0, s83
	v_lshl_add_u64 v[46:47], v[180:181], 0, s[28:29]
	v_lshl_add_u64 v[182:183], s[50:51], 0, v[166:167]
	s_add_u32 s6, s50, 0x20100
	ds_read_b128 v[38:41], v179 offset:16384
	ds_read_b128 v[42:45], v179 offset:17408
	ds_read_b128 v[54:57], v179 offset:18432
	ds_read_b128 v[58:61], v179 offset:19456
	ds_read_b128 v[190:193], v179 offset:20480
	ds_read_b128 v[194:197], v179 offset:21504
	ds_read_b128 v[212:215], v179 offset:22528
	ds_read_b128 v[216:219], v179 offset:23552
	global_load_lds_dwordx4 v[46:47], off
	v_lshl_add_u64 v[46:47], v[182:183], 0, s[28:29]
	s_mov_b32 m0, s84
	s_addc_u32 s7, s51, 0
	global_load_lds_dwordx4 v[46:47], off
	v_lshl_add_u64 v[46:47], s[6:7], 0, v[2:3]
	s_mov_b32 m0, s86
	v_lshl_add_u64 v[184:185], s[48:49], 0, v[168:169]
	global_load_lds_dwordx4 v[46:47], off
	v_lshl_add_u64 v[46:47], s[6:7], 0, v[166:167]
	s_mov_b32 m0, s87
	v_lshl_add_u64 v[186:187], s[48:49], 0, v[172:173]
	global_load_lds_dwordx4 v[46:47], off
	v_lshl_add_u64 v[46:47], v[184:185], 0, s[28:29]
	s_mov_b32 m0, s88
	s_nop 0
	global_load_lds_dwordx4 v[46:47], off
	v_lshl_add_u64 v[46:47], v[186:187], 0, s[28:29]
	s_mov_b32 m0, s89
	s_nop 0
	global_load_lds_dwordx4 v[46:47], off
	s_waitcnt vmcnt(8)
	s_waitcnt lgkmcnt(0)
	s_barrier
	s_setprio 1
	s_waitcnt lgkmcnt(0)
	v_mfma_f32_16x16x128_f8f6f4 v[114:117], v[6:13], v[38:45], 0
	v_mfma_f32_16x16x128_f8f6f4 v[110:113], v[14:21], v[38:45], 0
	v_mfma_f32_16x16x128_f8f6f4 v[82:85], v[6:13], v[54:61], 0
	v_mfma_f32_16x16x128_f8f6f4 v[78:81], v[14:21], v[54:61], 0
	v_mfma_f32_16x16x128_f8f6f4 v[66:69], v[6:13], v[190:197], 0
	v_mfma_f32_16x16x128_f8f6f4 v[62:65], v[14:21], v[190:197], 0
	v_mfma_f32_16x16x128_f8f6f4 v[50:53], v[6:13], v[212:219], 0
	v_mfma_f32_16x16x128_f8f6f4 v[46:49], v[14:21], v[212:219], 0
	s_setprio 0
	s_setprio 1
	v_mfma_f32_16x16x128_f8f6f4 v[102:105], v[22:29], v[38:45], 0
	v_mfma_f32_16x16x128_f8f6f4 v[94:97], v[30:37], v[38:45], 0
	v_mfma_f32_16x16x128_f8f6f4 v[74:77], v[22:29], v[54:61], 0
	v_mfma_f32_16x16x128_f8f6f4 v[70:73], v[30:37], v[54:61], 0
	v_mfma_f32_16x16x128_f8f6f4 v[58:61], v[22:29], v[190:197], 0
	v_mfma_f32_16x16x128_f8f6f4 v[54:57], v[30:37], v[190:197], 0
	v_mfma_f32_16x16x128_f8f6f4 v[42:45], v[22:29], v[212:219], 0
	v_mfma_f32_16x16x128_f8f6f4 v[38:41], v[30:37], v[212:219], 0
	s_setprio 0
	s_barrier
; #define PG8_STAGE(bufoff, gbase, voff) do { _Pragma("unroll") for (int _i = 0; _i < 2; ++_i) \
;         __builtin_amdgcn_global_load_lds((const unsigned*)((const char*)(gbase) + (voff)[_i]), (LAS unsigned*)(lds + (bufoff) + ldsw + _i * 8192), 16, 0, 0); } while (0)
; #define PG8_LDA(dst, b, h) do { if constexpr (F8) { _Pragma("unroll") for (int m = 0; m < 4; ++m) dst##8[m] = PG8_LD8(lds + PG8_SA(b, h) + aoff + m * 2048); } else { \
;         _Pragma("unroll") for (int m = 0; m < 4; ++m) _Pragma("unroll") for (int k = 0; k < 2; ++k) dst[m][k] = *(const LAS bf16x8*)(lds + PG8_SA(b, h) + aoff + m * 2048 + k * 1024); } } while (0)
; #define PG8_LDB(dst, b, h) do { if constexpr (F8) { _Pragma("unroll") for (int n = 0; n < 2; ++n) dst##8[n] = PG8_LD8(lds + PG8_SB(b, h) + boff + n * 2048); } else { \
;         _Pragma("unroll") for (int n = 0; n < 2; ++n) _Pragma("unroll") for (int k = 0; k < 2; ++k) dst[n][k] = *(const LAS bf16x8*)(lds + PG8_SB(b, h) + boff + n * 2048 + k * 1024); } } while (0)
; #define PG8_WAIT_V(n) asm volatile("s_waitcnt vmcnt(" #n ")" ::: "memory")
; #define PG8_WAIT_L(n) asm volatile("s_waitcnt lgkmcnt(" #n ")" ::: "memory")
; #define PG8_BAR __builtin_amdgcn_s_barrier()
; #define PG8_SCHED __builtin_amdgcn_sched_barrier(0)
; template <class Epi, class Sched, bool F8 = false>
; DI void gemm_phase(LAS unsigned char* lds, const int K, const Sched& S, const Epi& E) {
;     ...
;             PG8_LDB(B0, 1, 0); PG8_LDB(B1, 1, 1); PG8_SCHED; PG8_LDA(At, 1, 0); PG8_STAGE(PG8_SA(0, 1), a2, oA[1]);
;             PG8_WAIT_V(8); PG8_WAIT_L(0); PG8_BAR; PG8_MMA(0, 0, At, B0); PG8_MMA(0, 1, At, B1); PG8_BAR; PG8_SCHED;
;             PG8_LDA(At, 1, 1); PG8_STAGE(PG8_SB(1, 0), b3, voffB); PG8_STAGE(PG8_SB(1, 1), b3 + hstep, voffB); PG8_STAGE(PG8_SA(1, 0), a3, oA[0]);
;             PG8_WAIT_V(8); PG8_WAIT_L(0); PG8_BAR; PG8_MMA(1, 0, At, B0); PG8_MMA(1, 1, At, B1); PG8_BAR; PG8_SCHED;
;         }
	v_add_u32_e32 v190, s96, v177
	v_add_u32_e32 v191, s4, v177
	ds_read_b128 v[22:25], v190
	ds_read_b128 v[26:29], v190 offset:1024
	ds_read_b128 v[30:33], v190 offset:2048
	ds_read_b128 v[34:37], v190 offset:3072
	ds_read_b128 v[6:9], v191
	ds_read_b128 v[10:13], v191 offset:1024
	ds_read_b128 v[14:17], v191 offset:2048
	ds_read_b128 v[18:21], v191 offset:3072
	s_mov_b32 m0, s90
	v_lshl_add_u64 v[200:201], v[200:201], 0, s[28:29]
	ds_read_b128 v[192:195], v179 offset:32768
	ds_read_b128 v[196:199], v179 offset:33792
	ds_read_b128 v[212:215], v179 offset:34816
	ds_read_b128 v[216:219], v179 offset:35840
	ds_read_b128 v[226:229], v179 offset:36864
	ds_read_b128 v[230:233], v179 offset:37888
	ds_read_b128 v[236:239], v179 offset:38912
	ds_read_b128 v[240:243], v179 offset:39936
	global_load_lds_dwordx4 v[200:201], off
	v_lshl_add_u64 v[200:201], v[220:221], 0, s[28:29]
	s_mov_b32 m0, s91
	s_nop 0
	global_load_lds_dwordx4 v[200:201], off
	s_waitcnt vmcnt(8)
	s_waitcnt lgkmcnt(0)
	s_barrier
	s_setprio 1
	s_waitcnt lgkmcnt(0)
	v_mfma_f32_16x16x128_f8f6f4 v[162:165], v[22:29], v[192:199], v[162:165]
	v_mfma_f32_16x16x128_f8f6f4 v[158:161], v[30:37], v[192:199], v[158:161]
	v_mfma_f32_16x16x128_f8f6f4 v[146:149], v[22:29], v[212:219], v[146:149]
	v_mfma_f32_16x16x128_f8f6f4 v[142:145], v[30:37], v[212:219], v[142:145]
	v_mfma_f32_16x16x128_f8f6f4 v[130:133], v[22:29], v[226:233], v[130:133]
	v_mfma_f32_16x16x128_f8f6f4 v[126:129], v[30:37], v[226:233], v[126:129]
	v_mfma_f32_16x16x128_f8f6f4 v[106:109], v[22:29], v[236:243], v[106:109]
	v_mfma_f32_16x16x128_f8f6f4 v[98:101], v[30:37], v[236:243], v[98:101]
	s_setprio 0
	s_setprio 1
	v_mfma_f32_16x16x128_f8f6f4 v[154:157], v[6:13], v[192:199], v[154:157]
	v_mfma_f32_16x16x128_f8f6f4 v[150:153], v[14:21], v[192:199], v[150:153]
	v_mfma_f32_16x16x128_f8f6f4 v[138:141], v[6:13], v[212:219], v[138:141]
	v_mfma_f32_16x16x128_f8f6f4 v[134:137], v[14:21], v[212:219], v[134:137]
	v_mfma_f32_16x16x128_f8f6f4 v[122:125], v[6:13], v[226:233], v[122:125]
	v_mfma_f32_16x16x128_f8f6f4 v[118:121], v[14:21], v[226:233], v[118:121]
	v_mfma_f32_16x16x128_f8f6f4 v[90:93], v[6:13], v[236:243], v[90:93]
	v_mfma_f32_16x16x128_f8f6f4 v[86:89], v[14:21], v[236:243], v[86:89]
	s_setprio 0
	s_barrier
	s_mov_b32 m0, s5
	v_lshl_add_u64 v[180:181], v[180:181], 0, s[26:27]
	s_add_u32 s6, s50, 0x20180
	ds_read_b128 v[192:195], v179 offset:49152
	ds_read_b128 v[196:199], v179 offset:50176
	ds_read_b128 v[212:215], v179 offset:51200
	ds_read_b128 v[216:219], v179 offset:52224
	ds_read_b128 v[226:229], v179 offset:53248
	ds_read_b128 v[230:233], v179 offset:54272
	ds_read_b128 v[236:239], v179 offset:55296
	ds_read_b128 v[240:243], v179 offset:56320
	global_load_lds_dwordx4 v[180:181], off
	v_lshl_add_u64 v[180:181], v[182:183], 0, s[26:27]
	s_mov_b32 m0, s97
	s_addc_u32 s7, s51, 0
	global_load_lds_dwordx4 v[180:181], off
	v_lshl_add_u64 v[180:181], s[6:7], 0, v[2:3]
	s_mov_b32 m0, s79
	s_nop 0
	global_load_lds_dwordx4 v[180:181], off
	v_lshl_add_u64 v[180:181], s[6:7], 0, v[166:167]
	s_mov_b32 m0, s78
	s_nop 0
	global_load_lds_dwordx4 v[180:181], off
	v_lshl_add_u64 v[180:181], v[184:185], 0, s[26:27]
	s_mov_b32 m0, s80
	s_nop 0
	global_load_lds_dwordx4 v[180:181], off
	v_lshl_add_u64 v[180:181], v[186:187], 0, s[26:27]
	s_mov_b32 m0, s81
	s_nop 0
	global_load_lds_dwordx4 v[180:181], off
	s_waitcnt vmcnt(8)
	s_waitcnt lgkmcnt(0)
	s_barrier
	s_setprio 1
	s_waitcnt lgkmcnt(0)
	v_mfma_f32_16x16x128_f8f6f4 v[114:117], v[22:29], v[192:199], v[114:117]
	v_mfma_f32_16x16x128_f8f6f4 v[110:113], v[30:37], v[192:199], v[110:113]
	v_mfma_f32_16x16x128_f8f6f4 v[82:85], v[22:29], v[212:219], v[82:85]
	v_mfma_f32_16x16x128_f8f6f4 v[78:81], v[30:37], v[212:219], v[78:81]
	v_mfma_f32_16x16x128_f8f6f4 v[66:69], v[22:29], v[226:233], v[66:69]
	v_mfma_f32_16x16x128_f8f6f4 v[62:65], v[30:37], v[226:233], v[62:65]
	v_mfma_f32_16x16x128_f8f6f4 v[50:53], v[22:29], v[236:243], v[50:53]
	v_mfma_f32_16x16x128_f8f6f4 v[46:49], v[30:37], v[236:243], v[46:49]
	s_setprio 0
	s_setprio 1
	v_mfma_f32_16x16x128_f8f6f4 v[102:105], v[6:13], v[192:199], v[102:105]
	v_mfma_f32_16x16x128_f8f6f4 v[94:97], v[14:21], v[192:199], v[94:97]
	v_mfma_f32_16x16x128_f8f6f4 v[74:77], v[6:13], v[212:219], v[74:77]
	v_mfma_f32_16x16x128_f8f6f4 v[70:73], v[14:21], v[212:219], v[70:73]
	v_mfma_f32_16x16x128_f8f6f4 v[58:61], v[6:13], v[226:233], v[58:61]
	v_mfma_f32_16x16x128_f8f6f4 v[54:57], v[14:21], v[226:233], v[54:57]
	v_mfma_f32_16x16x128_f8f6f4 v[42:45], v[6:13], v[236:243], v[42:45]
	v_mfma_f32_16x16x128_f8f6f4 v[38:41], v[14:21], v[236:243], v[38:41]
	s_setprio 0
	s_barrier
	s_add_u32 s6, s50, 0x200
	s_addc_u32 s7, s51, 0
	s_add_u32 s48, s48, 0x180
	s_addc_u32 s49, s49, 0
	s_mov_b32 s55, 0
	.p2alignl 6, 3212836864
